# attention P.V on f32 MFMA (v_mfma_f32_4x4x1_16b_f32, same f32 fma chains) instead of 2048 VALU v_fmac per row task
# speedup vs baseline: 1.0386x; 1.0141x over previous
.LBB0_1236:
	s_or_b64 exec, exec, s[2:3]
	v_lshl_add_u64 v[70:71], v[116:117], 0, v[62:63]
	global_load_dwordx4 v[62:65], v[70:71], off offset:16
	s_nop 0
	global_load_dwordx4 v[70:73], v[70:71], off
	s_waitcnt lgkmcnt(14)
	v_cndmask_b32_e64 v86, v184, v204, s[6:7]
	v_cndmask_b32_e64 v184, v185, v205, s[6:7]
	s_waitcnt lgkmcnt(11)
	v_cndmask_b32_e64 v86, v86, v208, s[8:9]
	s_waitcnt lgkmcnt(10)
	v_cndmask_b32_e64 v184, v184, v209, s[8:9]
	s_waitcnt lgkmcnt(7)
	v_cndmask_b32_e64 v86, v86, v212, s[10:11]
	v_cndmask_b32_e64 v185, v186, v206, s[6:7]
	v_cndmask_b32_e64 v186, v187, v207, s[6:7]
	s_waitcnt lgkmcnt(6)
	v_cndmask_b32_e64 v187, v184, v213, s[10:11]
	s_waitcnt lgkmcnt(3)
	v_cndmask_b32_e64 v184, v86, v216, s[12:13]
	v_cndmask_b32_e64 v86, v179, v188, s[6:7]
	v_cndmask_b32_e64 v179, v180, v189, s[6:7]
	v_cndmask_b32_e64 v180, v181, v190, s[6:7]
	v_cndmask_b32_e64 v181, v182, v191, s[6:7]
	v_cndmask_b32_e64 v185, v185, v210, s[8:9]
	v_cndmask_b32_e64 v186, v186, v211, s[8:9]
	v_cndmask_b32_e64 v86, v86, v192, s[8:9]
	v_cndmask_b32_e64 v179, v179, v193, s[8:9]
	v_cndmask_b32_e64 v180, v180, v194, s[8:9]
	v_cndmask_b32_e64 v181, v181, v195, s[8:9]
	v_cndmask_b32_e64 v204, v185, v214, s[10:11]
	v_cndmask_b32_e64 v205, v186, v215, s[10:11]
	v_cndmask_b32_e64 v86, v86, v196, s[10:11]
	v_cndmask_b32_e64 v182, v179, v197, s[10:11]
	v_cndmask_b32_e64 v188, v180, v198, s[10:11]
	v_cndmask_b32_e64 v189, v181, v199, s[10:11]
	s_waitcnt lgkmcnt(2)
	v_cndmask_b32_e64 v185, v187, v217, s[12:13]
	s_waitcnt lgkmcnt(1)
	v_cndmask_b32_e64 v186, v204, v218, s[12:13]
	s_waitcnt lgkmcnt(0)
	v_cndmask_b32_e64 v187, v205, v219, s[12:13]
	v_cndmask_b32_e64 v179, v86, v200, s[12:13]
	v_cndmask_b32_e64 v180, v182, v201, s[12:13]
	v_cndmask_b32_e64 v181, v188, v202, s[12:13]
	v_cndmask_b32_e64 v182, v189, v203, s[12:13]
	s_waitcnt vmcnt(14)
	v_cvt_pk_f32_fp8_e32 v[188:189], v54
	v_cvt_pk_f32_fp8_sdwa v[190:191], v54 src0_sel:WORD_1
	v_cvt_pk_f32_fp8_e32 v[192:193], v55
	v_cvt_pk_bf16_f32 v188, v188, v189
	v_cvt_pk_bf16_f32 v189, v190, v191
	v_cvt_pk_bf16_f32 v190, v192, v193
	v_cvt_scalef32_pk_bf16_fp8 v191, v55, 1.0 op_sel:[1,0,0]
	s_nop 1
	v_mfma_f32_16x16x32_bf16 v[188:191], v[6:9], v[188:191], 0
	v_cvt_scalef32_pk_bf16_fp8 v54, v56, 1.0
	v_cvt_scalef32_pk_bf16_fp8 v55, v56, 1.0 op_sel:[1,0,0]
	v_cvt_scalef32_pk_bf16_fp8 v56, v57, 1.0
	v_cvt_scalef32_pk_bf16_fp8 v57, v57, 1.0 op_sel:[1,0,0]
	v_cvt_pk_f32_fp8_e32 v[192:193], v47
	s_mov_b32 s2, 0
	v_mfma_f32_16x16x32_bf16 v[54:57], v[2:5], v[54:57], v[188:191]
	s_nop 2
	v_cvt_pk_f32_fp8_e32 v[188:189], v46
	v_cvt_pk_f32_fp8_sdwa v[190:191], v46 src0_sel:WORD_1
	v_cvt_pk_bf16_f32 v188, v188, v189
	v_cvt_pk_bf16_f32 v189, v190, v191
	v_cvt_pk_bf16_f32 v190, v192, v193
	v_cvt_scalef32_pk_bf16_fp8 v191, v47, 1.0 op_sel:[1,0,0]
	s_nop 1
	v_mfma_f32_16x16x32_bf16 v[54:57], v[14:17], v[188:191], v[54:57]
	v_cvt_pk_f32_fp8_e32 v[190:191], v49
	v_cvt_scalef32_pk_bf16_fp8 v46, v48, 1.0
	v_cvt_scalef32_pk_bf16_fp8 v49, v49, 1.0 op_sel:[1,0,0]
	v_cvt_scalef32_pk_bf16_fp8 v47, v48, 1.0 op_sel:[1,0,0]
	v_cvt_pk_bf16_f32 v48, v190, v191
	s_nop 1
	s_nop 0
	v_mfma_f32_16x16x32_bf16 v[46:49], v[10:13], v[46:49], v[54:57]
	s_nop 7
	ds_bpermute_b32 v48, v166, v48
	ds_bpermute_b32 v49, v166, v49
	ds_bpermute_b32 v46, v166, v46
	ds_bpermute_b32 v47, v166, v47
	s_waitcnt lgkmcnt(3)
	v_cndmask_b32_e64 v178, v178, v48, s[6:7]
	s_waitcnt lgkmcnt(2)
	v_cndmask_b32_e64 v183, v183, v49, s[6:7]
	s_waitcnt lgkmcnt(1)
	v_cndmask_b32_e64 v86, v176, v46, s[6:7]
	s_waitcnt lgkmcnt(0)
	v_cndmask_b32_e64 v188, v177, v47, s[6:7]
	s_waitcnt vmcnt(12)
	v_cvt_pk_f32_fp8_e32 v[46:47], v38
	v_cvt_pk_f32_fp8_sdwa v[48:49], v38 src0_sel:WORD_1
	v_cvt_pk_f32_fp8_e32 v[54:55], v39
	v_cvt_pk_bf16_f32 v46, v46, v47
	v_cvt_pk_bf16_f32 v47, v48, v49
	v_cvt_pk_bf16_f32 v48, v54, v55
	v_cvt_scalef32_pk_bf16_fp8 v49, v39, 1.0 op_sel:[1,0,0]
	s_nop 1
	v_mfma_f32_16x16x32_bf16 v[46:49], v[6:9], v[46:49], 0
	v_cvt_scalef32_pk_bf16_fp8 v38, v40, 1.0
	v_cvt_scalef32_pk_bf16_fp8 v39, v40, 1.0 op_sel:[1,0,0]
	v_cvt_scalef32_pk_bf16_fp8 v40, v41, 1.0
	v_cvt_scalef32_pk_bf16_fp8 v41, v41, 1.0 op_sel:[1,0,0]
	v_cvt_pk_f32_fp8_e32 v[54:55], v35
	s_nop 0
	v_mfma_f32_16x16x32_bf16 v[38:41], v[2:5], v[38:41], v[46:49]
	s_nop 2
	v_cvt_pk_f32_fp8_e32 v[46:47], v34
	v_cvt_pk_f32_fp8_sdwa v[48:49], v34 src0_sel:WORD_1
	v_cvt_pk_bf16_f32 v46, v46, v47
	v_cvt_pk_bf16_f32 v47, v48, v49
	v_cvt_pk_bf16_f32 v48, v54, v55
	v_cvt_scalef32_pk_bf16_fp8 v49, v35, 1.0 op_sel:[1,0,0]
	s_nop 1
	v_mfma_f32_16x16x32_bf16 v[38:41], v[14:17], v[46:49], v[38:41]
	v_cvt_pk_f32_fp8_e32 v[48:49], v37
	v_cvt_scalef32_pk_bf16_fp8 v34, v36, 1.0
	v_cvt_scalef32_pk_bf16_fp8 v37, v37, 1.0 op_sel:[1,0,0]
	v_cvt_scalef32_pk_bf16_fp8 v35, v36, 1.0 op_sel:[1,0,0]
	v_cvt_pk_bf16_f32 v36, v48, v49
	s_nop 1
	s_nop 0
	v_mfma_f32_16x16x32_bf16 v[34:37], v[10:13], v[34:37], v[38:41]
	s_nop 7
	ds_bpermute_b32 v34, v166, v34
	ds_bpermute_b32 v35, v166, v35
	ds_bpermute_b32 v36, v166, v36
	ds_bpermute_b32 v37, v166, v37
	s_waitcnt lgkmcnt(3)
	v_cndmask_b32_e64 v48, v86, v34, s[8:9]
	s_waitcnt lgkmcnt(2)
	v_cndmask_b32_e64 v49, v188, v35, s[8:9]
	s_waitcnt lgkmcnt(1)
	v_cndmask_b32_e64 v54, v178, v36, s[8:9]
	s_waitcnt lgkmcnt(0)
	v_cndmask_b32_e64 v55, v183, v37, s[8:9]
	s_waitcnt vmcnt(10)
	v_cvt_pk_f32_fp8_e32 v[34:35], v30
	v_cvt_pk_f32_fp8_sdwa v[36:37], v30 src0_sel:WORD_1
	v_cvt_pk_f32_fp8_e32 v[38:39], v31
	v_cvt_pk_bf16_f32 v34, v34, v35
	v_cvt_pk_bf16_f32 v35, v36, v37
	v_cvt_pk_bf16_f32 v36, v38, v39
	v_cvt_scalef32_pk_bf16_fp8 v37, v31, 1.0 op_sel:[1,0,0]
	s_nop 1
	v_mfma_f32_16x16x32_bf16 v[34:37], v[6:9], v[34:37], 0
	v_cvt_scalef32_pk_bf16_fp8 v30, v32, 1.0
	v_cvt_scalef32_pk_bf16_fp8 v31, v32, 1.0 op_sel:[1,0,0]
	v_cvt_scalef32_pk_bf16_fp8 v32, v33, 1.0
	v_cvt_scalef32_pk_bf16_fp8 v33, v33, 1.0 op_sel:[1,0,0]
	v_cvt_pk_f32_fp8_e32 v[38:39], v23
	s_nop 0
	v_mfma_f32_16x16x32_bf16 v[30:33], v[2:5], v[30:33], v[34:37]
	s_nop 2
	v_cvt_pk_f32_fp8_e32 v[34:35], v22
	v_cvt_pk_f32_fp8_sdwa v[36:37], v22 src0_sel:WORD_1
	v_cvt_pk_bf16_f32 v34, v34, v35
	v_cvt_pk_bf16_f32 v35, v36, v37
	v_cvt_pk_bf16_f32 v36, v38, v39
	v_cvt_scalef32_pk_bf16_fp8 v37, v23, 1.0 op_sel:[1,0,0]
	s_nop 1
	v_mfma_f32_16x16x32_bf16 v[30:33], v[14:17], v[34:37], v[30:33]
	v_cvt_pk_f32_fp8_e32 v[36:37], v25
	v_cvt_scalef32_pk_bf16_fp8 v22, v24, 1.0
	v_cvt_scalef32_pk_bf16_fp8 v25, v25, 1.0 op_sel:[1,0,0]
	v_cvt_scalef32_pk_bf16_fp8 v23, v24, 1.0 op_sel:[1,0,0]
	v_cvt_pk_bf16_f32 v24, v36, v37
	s_nop 1
	s_nop 0
	v_mfma_f32_16x16x32_bf16 v[22:25], v[10:13], v[22:25], v[30:33]
	s_nop 7
	ds_bpermute_b32 v22, v166, v22
	ds_bpermute_b32 v23, v166, v23
	ds_bpermute_b32 v24, v166, v24
	ds_bpermute_b32 v25, v166, v25
	s_waitcnt lgkmcnt(3)
	v_cndmask_b32_e64 v36, v48, v22, s[10:11]
	s_waitcnt lgkmcnt(2)
	v_cndmask_b32_e64 v37, v49, v23, s[10:11]
	s_waitcnt lgkmcnt(1)
	v_cndmask_b32_e64 v38, v54, v24, s[10:11]
	s_waitcnt lgkmcnt(0)
	v_cndmask_b32_e64 v39, v55, v25, s[10:11]
	s_waitcnt vmcnt(8)
	v_cvt_pk_f32_fp8_e32 v[22:23], v26
	v_cvt_pk_f32_fp8_sdwa v[24:25], v26 src0_sel:WORD_1
	v_cvt_pk_f32_fp8_e32 v[30:31], v27
	v_cvt_pk_bf16_f32 v22, v22, v23
	v_cvt_pk_bf16_f32 v23, v24, v25
	v_cvt_pk_bf16_f32 v24, v30, v31
	v_cvt_scalef32_pk_bf16_fp8 v25, v27, 1.0 op_sel:[1,0,0]
	s_nop 1
	v_mfma_f32_16x16x32_bf16 v[22:25], v[6:9], v[22:25], 0
	v_cvt_scalef32_pk_bf16_fp8 v26, v28, 1.0
	v_cvt_scalef32_pk_bf16_fp8 v27, v28, 1.0 op_sel:[1,0,0]
	v_cvt_scalef32_pk_bf16_fp8 v28, v29, 1.0
	v_cvt_scalef32_pk_bf16_fp8 v29, v29, 1.0 op_sel:[1,0,0]
	v_cvt_pk_f32_fp8_e32 v[30:31], v19
	s_nop 0
	v_mfma_f32_16x16x32_bf16 v[22:25], v[2:5], v[26:29], v[22:25]
	v_cvt_pk_f32_fp8_e32 v[26:27], v18
	v_cvt_pk_f32_fp8_sdwa v[28:29], v18 src0_sel:WORD_1
	v_cvt_pk_bf16_f32 v26, v26, v27
	v_cvt_pk_bf16_f32 v27, v28, v29
	v_cvt_pk_bf16_f32 v28, v30, v31
	v_cvt_scalef32_pk_bf16_fp8 v29, v19, 1.0 op_sel:[1,0,0]
	s_nop 1
	v_mfma_f32_16x16x32_bf16 v[22:25], v[14:17], v[26:29], v[22:25]
	v_cvt_pk_f32_fp8_e32 v[28:29], v21
	v_cvt_scalef32_pk_bf16_fp8 v18, v20, 1.0
	v_cvt_scalef32_pk_bf16_fp8 v21, v21, 1.0 op_sel:[1,0,0]
	v_cvt_scalef32_pk_bf16_fp8 v19, v20, 1.0 op_sel:[1,0,0]
	v_cvt_pk_bf16_f32 v20, v28, v29
	s_nop 1
	s_nop 0
	v_mfma_f32_16x16x32_bf16 v[18:21], v[10:13], v[18:21], v[22:25]
	s_nop 7
	ds_bpermute_b32 v18, v166, v18
	ds_bpermute_b32 v19, v166, v19
	ds_bpermute_b32 v20, v166, v20
	ds_bpermute_b32 v21, v166, v21
	s_waitcnt lgkmcnt(3)
	v_cndmask_b32_e64 v36, v36, v18, s[12:13]
	s_waitcnt lgkmcnt(2)
	v_cndmask_b32_e64 v37, v37, v19, s[12:13]
	s_waitcnt lgkmcnt(1)
	v_cndmask_b32_e64 v38, v38, v20, s[12:13]
	s_waitcnt lgkmcnt(0)
	v_cndmask_b32_e64 v39, v39, v21, s[12:13]
	s_waitcnt vmcnt(6)
	v_cvt_scalef32_pk_bf16_fp8 v18, v78, 1.0
	v_cvt_scalef32_pk_bf16_fp8 v19, v78, 1.0 op_sel:[1,0,0]
	v_cvt_scalef32_pk_bf16_fp8 v20, v79, 1.0
	v_cvt_scalef32_pk_bf16_fp8 v21, v79, 1.0 op_sel:[1,0,0]
	s_nop 1
	v_mfma_f32_16x16x32_bf16 v[18:21], v[6:9], v[18:21], 0
	v_cvt_scalef32_pk_bf16_fp8 v22, v80, 1.0
	v_cvt_scalef32_pk_bf16_fp8 v23, v80, 1.0 op_sel:[1,0,0]
	v_cvt_scalef32_pk_bf16_fp8 v24, v81, 1.0
	v_cvt_scalef32_pk_bf16_fp8 v25, v81, 1.0 op_sel:[1,0,0]
	s_nop 1
	v_mfma_f32_16x16x32_bf16 v[18:21], v[2:5], v[22:25], v[18:21]
	v_cvt_scalef32_pk_bf16_fp8 v22, v74, 1.0
	v_cvt_scalef32_pk_bf16_fp8 v23, v74, 1.0 op_sel:[1,0,0]
	v_cvt_scalef32_pk_bf16_fp8 v24, v75, 1.0
	v_cvt_scalef32_pk_bf16_fp8 v25, v75, 1.0 op_sel:[1,0,0]
	s_nop 1
	v_mfma_f32_16x16x32_bf16 v[18:21], v[14:17], v[22:25], v[18:21]
	v_cvt_scalef32_pk_bf16_fp8 v22, v76, 1.0
	v_cvt_scalef32_pk_bf16_fp8 v23, v76, 1.0 op_sel:[1,0,0]
	v_cvt_scalef32_pk_bf16_fp8 v24, v77, 1.0
	v_cvt_scalef32_pk_bf16_fp8 v25, v77, 1.0 op_sel:[1,0,0]
	s_nop 1
	s_nop 0
	v_mfma_f32_16x16x32_bf16 v[18:21], v[10:13], v[22:25], v[18:21]
	s_nop 7
	ds_bpermute_b32 v18, v166, v18
	ds_bpermute_b32 v19, v166, v19
	ds_bpermute_b32 v20, v166, v20
	ds_bpermute_b32 v21, v166, v21
	s_waitcnt lgkmcnt(3)
	v_cndmask_b32_e64 v30, v165, v18, s[6:7]
	s_waitcnt lgkmcnt(2)
	v_cndmask_b32_e64 v31, v169, v19, s[6:7]
	s_waitcnt lgkmcnt(1)
	v_cndmask_b32_e64 v32, v174, v20, s[6:7]
	s_waitcnt lgkmcnt(0)
	v_cndmask_b32_e64 v33, v175, v21, s[6:7]
	s_waitcnt vmcnt(4)
	v_cvt_scalef32_pk_bf16_fp8 v18, v66, 1.0
	v_cvt_scalef32_pk_bf16_fp8 v19, v66, 1.0 op_sel:[1,0,0]
	v_cvt_scalef32_pk_bf16_fp8 v20, v67, 1.0
	v_cvt_scalef32_pk_bf16_fp8 v21, v67, 1.0 op_sel:[1,0,0]
	s_nop 1
	v_mfma_f32_16x16x32_bf16 v[18:21], v[6:9], v[18:21], 0
	v_cvt_scalef32_pk_bf16_fp8 v22, v68, 1.0
	v_cvt_scalef32_pk_bf16_fp8 v23, v68, 1.0 op_sel:[1,0,0]
	v_cvt_scalef32_pk_bf16_fp8 v24, v69, 1.0
	v_cvt_scalef32_pk_bf16_fp8 v25, v69, 1.0 op_sel:[1,0,0]
	s_nop 1
	v_mfma_f32_16x16x32_bf16 v[18:21], v[2:5], v[22:25], v[18:21]
	v_cvt_scalef32_pk_bf16_fp8 v22, v58, 1.0
	v_cvt_scalef32_pk_bf16_fp8 v23, v58, 1.0 op_sel:[1,0,0]
	v_cvt_scalef32_pk_bf16_fp8 v24, v59, 1.0
	v_cvt_scalef32_pk_bf16_fp8 v25, v59, 1.0 op_sel:[1,0,0]
	s_nop 1
	v_mfma_f32_16x16x32_bf16 v[18:21], v[14:17], v[22:25], v[18:21]
	v_cvt_scalef32_pk_bf16_fp8 v22, v60, 1.0
	v_cvt_scalef32_pk_bf16_fp8 v23, v60, 1.0 op_sel:[1,0,0]
	v_cvt_scalef32_pk_bf16_fp8 v24, v61, 1.0
	v_cvt_scalef32_pk_bf16_fp8 v25, v61, 1.0 op_sel:[1,0,0]
	s_nop 1
	s_nop 0
	v_mfma_f32_16x16x32_bf16 v[18:21], v[10:13], v[22:25], v[18:21]
	s_nop 7
	ds_bpermute_b32 v18, v166, v18
	ds_bpermute_b32 v19, v166, v19
	ds_bpermute_b32 v20, v166, v20
	ds_bpermute_b32 v21, v166, v21
	s_waitcnt lgkmcnt(3)
	v_cndmask_b32_e64 v30, v30, v18, s[8:9]
	s_waitcnt lgkmcnt(2)
	v_cndmask_b32_e64 v31, v31, v19, s[8:9]
	s_waitcnt lgkmcnt(1)
	v_cndmask_b32_e64 v32, v32, v20, s[8:9]
	s_waitcnt lgkmcnt(0)
	v_cndmask_b32_e64 v33, v33, v21, s[8:9]
	s_waitcnt vmcnt(2)
	v_cvt_scalef32_pk_bf16_fp8 v18, v50, 1.0
	v_cvt_scalef32_pk_bf16_fp8 v19, v50, 1.0 op_sel:[1,0,0]
	v_cvt_scalef32_pk_bf16_fp8 v20, v51, 1.0
	v_cvt_scalef32_pk_bf16_fp8 v21, v51, 1.0 op_sel:[1,0,0]
	s_nop 1
	v_mfma_f32_16x16x32_bf16 v[18:21], v[6:9], v[18:21], 0
	v_cvt_scalef32_pk_bf16_fp8 v22, v52, 1.0
	v_cvt_scalef32_pk_bf16_fp8 v23, v52, 1.0 op_sel:[1,0,0]
	v_cvt_scalef32_pk_bf16_fp8 v24, v53, 1.0
	v_cvt_scalef32_pk_bf16_fp8 v25, v53, 1.0 op_sel:[1,0,0]
	s_nop 1
	v_mfma_f32_16x16x32_bf16 v[18:21], v[2:5], v[22:25], v[18:21]
	v_cvt_scalef32_pk_bf16_fp8 v22, v42, 1.0
	v_cvt_scalef32_pk_bf16_fp8 v23, v42, 1.0 op_sel:[1,0,0]
	v_cvt_scalef32_pk_bf16_fp8 v24, v43, 1.0
	v_cvt_scalef32_pk_bf16_fp8 v25, v43, 1.0 op_sel:[1,0,0]
	s_nop 1
	v_mfma_f32_16x16x32_bf16 v[18:21], v[14:17], v[22:25], v[18:21]
	v_cvt_scalef32_pk_bf16_fp8 v22, v44, 1.0
	v_cvt_scalef32_pk_bf16_fp8 v23, v44, 1.0 op_sel:[1,0,0]
	v_cvt_scalef32_pk_bf16_fp8 v24, v45, 1.0
	v_cvt_scalef32_pk_bf16_fp8 v25, v45, 1.0 op_sel:[1,0,0]
	s_nop 1
	s_nop 0
	v_mfma_f32_16x16x32_bf16 v[18:21], v[10:13], v[22:25], v[18:21]
	s_nop 7
	ds_bpermute_b32 v18, v166, v18
	ds_bpermute_b32 v19, v166, v19
	ds_bpermute_b32 v20, v166, v20
	ds_bpermute_b32 v21, v166, v21
	s_waitcnt lgkmcnt(3)
	v_cndmask_b32_e64 v26, v30, v18, s[10:11]
	s_waitcnt lgkmcnt(2)
	v_cndmask_b32_e64 v27, v31, v19, s[10:11]
	s_waitcnt lgkmcnt(1)
	v_cndmask_b32_e64 v28, v32, v20, s[10:11]
	s_waitcnt lgkmcnt(0)
	v_cndmask_b32_e64 v29, v33, v21, s[10:11]
	s_waitcnt vmcnt(0)
	v_cvt_scalef32_pk_bf16_fp8 v18, v70, 1.0
	v_cvt_scalef32_pk_bf16_fp8 v19, v70, 1.0 op_sel:[1,0,0]
	v_cvt_scalef32_pk_bf16_fp8 v20, v71, 1.0
	v_cvt_scalef32_pk_bf16_fp8 v21, v71, 1.0 op_sel:[1,0,0]
	s_nop 1
	v_mfma_f32_16x16x32_bf16 v[6:9], v[6:9], v[18:21], 0
	v_cvt_scalef32_pk_bf16_fp8 v18, v72, 1.0
	v_cvt_scalef32_pk_bf16_fp8 v19, v72, 1.0 op_sel:[1,0,0]
	v_cvt_scalef32_pk_bf16_fp8 v20, v73, 1.0
	v_cvt_scalef32_pk_bf16_fp8 v21, v73, 1.0 op_sel:[1,0,0]
	s_nop 1
	s_nop 0
	v_mfma_f32_16x16x32_bf16 v[2:5], v[2:5], v[18:21], v[6:9]
	s_nop 0
	v_cvt_scalef32_pk_bf16_fp8 v6, v62, 1.0
	v_cvt_scalef32_pk_bf16_fp8 v7, v62, 1.0 op_sel:[1,0,0]
	v_cvt_scalef32_pk_bf16_fp8 v8, v63, 1.0
	v_cvt_scalef32_pk_bf16_fp8 v9, v63, 1.0 op_sel:[1,0,0]
	s_nop 1
	s_nop 0
	v_mfma_f32_16x16x32_bf16 v[2:5], v[14:17], v[6:9], v[2:5]
	v_cvt_scalef32_pk_bf16_fp8 v6, v64, 1.0
	v_cvt_scalef32_pk_bf16_fp8 v7, v64, 1.0 op_sel:[1,0,0]
	v_cvt_scalef32_pk_bf16_fp8 v8, v65, 1.0
	v_cvt_scalef32_pk_bf16_fp8 v9, v65, 1.0 op_sel:[1,0,0]
	s_nop 1
	s_nop 0
	v_mfma_f32_16x16x32_bf16 v[2:5], v[10:13], v[6:9], v[2:5]
	s_nop 7
	ds_bpermute_b32 v2, v166, v2
	ds_bpermute_b32 v3, v166, v3
	ds_bpermute_b32 v4, v166, v4
	ds_bpermute_b32 v5, v166, v5
	s_waitcnt lgkmcnt(3)
	v_cndmask_b32_e64 v40, v26, v2, s[12:13]
	s_waitcnt lgkmcnt(2)
	v_cndmask_b32_e64 v41, v27, v3, s[12:13]
	s_waitcnt lgkmcnt(1)
	v_cndmask_b32_e64 v42, v28, v4, s[12:13]
	s_waitcnt lgkmcnt(0)
	v_cndmask_b32_e64 v43, v29, v5, s[12:13]
	ds_read_u16 v2, v142 offset:32768
	ds_read_u16 v4, v142 offset:32776
	ds_read_u16 v6, v142 offset:32784
	ds_read_u16 v8, v142 offset:32792
	ds_read_u16 v10, v142 offset:32800
	ds_read_u16 v12, v142 offset:32808
	ds_read_u16 v14, v142 offset:32816
	ds_read_u16 v16, v142 offset:32824
	s_waitcnt lgkmcnt(7)
	v_lshlrev_b32_e32 v86, 9, v2
	v_lshl_add_u64 v[2:3], v[118:119], 0, v[86:87]
	s_waitcnt lgkmcnt(6)
	v_lshlrev_b32_e32 v86, 9, v4
	v_lshl_add_u64 v[4:5], v[118:119], 0, v[86:87]
	s_waitcnt lgkmcnt(5)
	v_lshlrev_b32_e32 v86, 9, v6
	v_lshl_add_u64 v[6:7], v[118:119], 0, v[86:87]
	s_waitcnt lgkmcnt(4)
	v_lshlrev_b32_e32 v86, 9, v8
	v_lshl_add_u64 v[8:9], v[118:119], 0, v[86:87]
	s_waitcnt lgkmcnt(3)
	v_lshlrev_b32_e32 v86, 9, v10
	v_lshl_add_u64 v[10:11], v[118:119], 0, v[86:87]
	s_waitcnt lgkmcnt(2)
	v_lshlrev_b32_e32 v86, 9, v12
	v_lshl_add_u64 v[12:13], v[118:119], 0, v[86:87]
	s_waitcnt lgkmcnt(1)
	v_lshlrev_b32_e32 v86, 9, v14
	v_lshl_add_u64 v[14:15], v[118:119], 0, v[86:87]
	s_waitcnt lgkmcnt(0)
	v_lshlrev_b32_e32 v86, 9, v16
	v_lshl_add_u64 v[16:17], v[118:119], 0, v[86:87]
	global_load_dwordx2 v[2:3], v[2:3], off offset:128
	s_nop 0
	global_load_dwordx2 v[4:5], v[4:5], off offset:128
	s_nop 0
	global_load_dwordx2 v[6:7], v[6:7], off offset:128
	s_nop 0
	global_load_dwordx2 v[8:9], v[8:9], off offset:128
	s_nop 0
	global_load_dwordx2 v[10:11], v[10:11], off offset:128
	s_nop 0
	global_load_dwordx2 v[12:13], v[12:13], off offset:128
	s_nop 0
	global_load_dwordx2 v[14:15], v[14:15], off offset:128
	s_nop 0
	global_load_dwordx2 v[16:17], v[16:17], off offset:128
	ds_read_u16 v18, v142 offset:32832
	ds_read_u16 v20, v142 offset:32840
	ds_read_u16 v22, v142 offset:32848
	ds_read_u16 v24, v142 offset:32856
	ds_read_u16 v26, v142 offset:32864
	ds_read_u16 v28, v142 offset:32872
	ds_read_u16 v29, v142 offset:32880
	ds_read_u16 v34, v142 offset:32888
	s_waitcnt lgkmcnt(7)
	v_lshlrev_b32_e32 v86, 9, v18
	v_lshl_add_u64 v[18:19], v[118:119], 0, v[86:87]
	s_waitcnt lgkmcnt(6)
	v_lshlrev_b32_e32 v86, 9, v20
	v_lshl_add_u64 v[20:21], v[118:119], 0, v[86:87]
	s_waitcnt lgkmcnt(5)
	v_lshlrev_b32_e32 v86, 9, v22
	v_lshl_add_u64 v[22:23], v[118:119], 0, v[86:87]
	s_waitcnt lgkmcnt(4)
	v_lshlrev_b32_e32 v86, 9, v24
	v_lshl_add_u64 v[24:25], v[118:119], 0, v[86:87]
	s_waitcnt lgkmcnt(3)
	v_lshlrev_b32_e32 v86, 9, v26
	v_lshl_add_u64 v[26:27], v[118:119], 0, v[86:87]
	s_waitcnt lgkmcnt(2)
	v_lshlrev_b32_e32 v86, 9, v28
	v_lshl_add_u64 v[30:31], v[118:119], 0, v[86:87]
	s_waitcnt lgkmcnt(1)
	v_lshlrev_b32_e32 v86, 9, v29
	v_lshl_add_u64 v[32:33], v[118:119], 0, v[86:87]
	s_waitcnt lgkmcnt(0)
	v_lshlrev_b32_e32 v86, 9, v34
	v_lshl_add_u64 v[34:35], v[118:119], 0, v[86:87]
	global_load_dwordx2 v[18:19], v[18:19], off offset:128
	s_nop 0
	global_load_dwordx2 v[20:21], v[20:21], off offset:128
	s_nop 0
	global_load_dwordx2 v[22:23], v[22:23], off offset:128
	s_nop 0
	global_load_dwordx2 v[24:25], v[24:25], off offset:128
	s_nop 0
	global_load_dwordx2 v[28:29], v[26:27], off offset:128
	s_nop 0
	global_load_dwordx2 v[30:31], v[30:31], off offset:128
	s_nop 0
	global_load_dwordx2 v[32:33], v[32:33], off offset:128
	s_nop 0
	global_load_dwordx2 v[34:35], v[34:35], off offset:128
	s_add_i32 s3, s20, 4
	v_mul_f32_e32 v26, 0x3db504f3, v179
	v_cmp_lt_u32_e32 vcc, s14, v1
	v_mul_f32_e32 v27, 0x3db504f3, v36
	v_cmp_lt_u32_e64 s[14:15], s20, v160
	v_cndmask_b32_e32 v179, v26, v164, vcc
	v_mul_f32_e32 v26, 0x3db504f3, v180
	v_cndmask_b32_e32 v180, v26, v164, vcc
	v_mul_f32_e32 v26, 0x3db504f3, v181
	v_cndmask_b32_e32 v181, v26, v164, vcc
	v_mul_f32_e32 v26, 0x3db504f3, v182
	v_cndmask_b32_e64 v176, v27, v164, s[14:15]
	v_mul_f32_e32 v27, 0x3db504f3, v40
	v_cmp_lt_u32_e64 s[16:17], s20, v161
	v_cndmask_b32_e32 v182, v26, v164, vcc
	v_mul_f32_e32 v26, 0x3db504f3, v184
	v_cmp_lt_u32_e32 vcc, s20, v159
	v_cndmask_b32_e64 v165, v27, v164, s[16:17]
	v_max_f32_e32 v27, v176, v165
	v_cndmask_b32_e32 v184, v26, v164, vcc
	v_max3_f32 v27, v179, v184, v27
	ds_bpermute_b32 v36, v167, v27
	v_mul_f32_e32 v26, 0x3db504f3, v185
	v_cndmask_b32_e32 v185, v26, v164, vcc
	v_mul_f32_e32 v26, 0x3db504f3, v186
	v_cndmask_b32_e32 v186, v26, v164, vcc
	s_waitcnt lgkmcnt(0)
	v_max_f32_e32 v36, v36, v36
	v_max_f32_e32 v27, v27, v36
	ds_bpermute_b32 v36, v168, v27
	v_mul_f32_e32 v26, 0x3db504f3, v187
	v_cndmask_b32_e32 v187, v26, v164, vcc
	v_mul_f32_e32 v26, 0x3db504f3, v37
	v_mul_f32_e32 v37, 0x3db504f3, v41
	v_cndmask_b32_e64 v177, v26, v164, s[14:15]
	v_cndmask_b32_e64 v169, v37, v164, s[16:17]
	s_waitcnt lgkmcnt(0)
	v_max_f32_e32 v36, v36, v36
	v_max_f32_e32 v27, v27, v36
	v_max_f32_e32 v37, v177, v169
	ds_bpermute_b32 v36, v170, v27
	v_max3_f32 v37, v180, v185, v37
	v_mul_f32_e32 v26, 0x3db504f3, v38
	ds_bpermute_b32 v38, v167, v37
	v_cndmask_b32_e64 v178, v26, v164, s[14:15]
	v_mul_f32_e32 v26, 0x3db504f3, v39
	v_cndmask_b32_e64 v183, v26, v164, s[14:15]
	s_waitcnt lgkmcnt(1)
	v_max_f32_e32 v26, v36, v36
	v_max_f32_e32 v26, v27, v26
	s_waitcnt lgkmcnt(0)
	v_max_f32_e32 v36, v38, v38
	ds_bpermute_b32 v27, v171, v26
	v_max_f32_e32 v36, v37, v36
	ds_bpermute_b32 v37, v168, v36
	v_mul_f32_e32 v38, 0x3db504f3, v42
	v_cndmask_b32_e64 v174, v38, v164, s[16:17]
	s_waitcnt lgkmcnt(1)
	v_max_f32_e32 v27, v27, v27
	v_max_f32_e32 v26, v26, v27
	s_waitcnt lgkmcnt(0)
	v_max_f32_e32 v37, v37, v37
	ds_bpermute_b32 v27, v172, v26
	v_max_f32_e32 v36, v36, v37
	ds_bpermute_b32 v37, v170, v36
	v_mul_f32_e32 v38, 0x3db504f3, v43
	v_cndmask_b32_e64 v175, v38, v164, s[16:17]
	s_waitcnt lgkmcnt(1)
	v_max_f32_e32 v27, v27, v27
	v_max_f32_e32 v26, v26, v27
	s_waitcnt lgkmcnt(0)
	v_max_f32_e32 v37, v37, v37
	ds_bpermute_b32 v27, v173, v26
	v_max_f32_e32 v36, v36, v37
	ds_bpermute_b32 v37, v171, v36
	v_max_f32_e32 v39, v183, v175
	v_max3_f32 v39, v182, v187, v39
	s_waitcnt lgkmcnt(1)
	v_max_f32_e32 v27, v27, v27
	v_max_f32_e32 v26, v26, v27
	s_waitcnt lgkmcnt(0)
	v_max_f32_e32 v27, v37, v37
	v_max_f32_e32 v37, v178, v174
	v_max3_f32 v37, v181, v186, v37
	ds_bpermute_b32 v38, v167, v37
	ds_bpermute_b32 v40, v167, v39
	v_max_f32_e32 v27, v36, v27
	s_lshr_b32 s3, s3, 2
	s_mov_b32 s16, 32
	s_waitcnt lgkmcnt(1)
	v_max_f32_e32 v36, v38, v38
	v_max_f32_e32 v36, v37, v36
	s_waitcnt lgkmcnt(0)
	v_max_f32_e32 v38, v40, v40
	ds_bpermute_b32 v37, v168, v36
	v_max_f32_e32 v38, v39, v38
	ds_bpermute_b32 v39, v168, v38
	ds_bpermute_b32 v40, v172, v27
	v_mov_b32_e32 v74, v140
	s_waitcnt lgkmcnt(2)
	v_max_f32_e32 v37, v37, v37
	v_max_f32_e32 v36, v36, v37
	s_waitcnt lgkmcnt(1)
	v_max_f32_e32 v39, v39, v39
	ds_bpermute_b32 v37, v170, v36
	v_max_f32_e32 v38, v38, v39
	ds_bpermute_b32 v39, v170, v38
	s_waitcnt lgkmcnt(2)
	v_max_f32_e32 v40, v40, v40
	v_max_f32_e32 v27, v27, v40
	s_waitcnt lgkmcnt(1)
	v_max_f32_e32 v37, v37, v37
	v_max_f32_e32 v36, v36, v37
	s_waitcnt lgkmcnt(0)
	v_max_f32_e32 v39, v39, v39
	ds_bpermute_b32 v37, v171, v36
	v_max_f32_e32 v38, v38, v39
	ds_bpermute_b32 v39, v171, v38
	ds_bpermute_b32 v40, v173, v27
	s_waitcnt lgkmcnt(2)
	v_max_f32_e32 v37, v37, v37
	v_max_f32_e32 v36, v36, v37
	s_waitcnt lgkmcnt(1)
	v_max_f32_e32 v39, v39, v39
	ds_bpermute_b32 v37, v172, v36
	v_max_f32_e32 v38, v38, v39
	ds_bpermute_b32 v39, v172, v38
	s_waitcnt lgkmcnt(2)
	v_max_f32_e32 v40, v40, v40
	v_max_f32_e32 v27, v27, v40
	s_waitcnt lgkmcnt(1)
	v_max_f32_e32 v37, v37, v37
	v_max_f32_e32 v36, v36, v37
	s_waitcnt lgkmcnt(0)
	v_max_f32_e32 v39, v39, v39
	ds_bpermute_b32 v37, v173, v36
	v_max_f32_e32 v38, v38, v39
	ds_bpermute_b32 v39, v173, v38
	v_sub_f32_e32 v40, v184, v26
	v_mul_f32_e32 v40, 0x3fb8aa3b, v40
	s_waitcnt lgkmcnt(1)
	v_max_f32_e32 v37, v37, v37
	v_max_f32_e32 v44, v36, v37
	s_waitcnt lgkmcnt(0)
	v_max_f32_e32 v36, v39, v39
	v_max_f32_e32 v45, v38, v36
	v_sub_f32_e32 v36, v179, v26
	v_sub_f32_e32 v37, v180, v27
	v_sub_f32_e32 v38, v181, v44
	v_sub_f32_e32 v39, v182, v45
	v_mul_f32_e32 v36, 0x3fb8aa3b, v36
	v_mul_f32_e32 v37, 0x3fb8aa3b, v37
	v_mul_f32_e32 v38, 0x3fb8aa3b, v38
	v_mul_f32_e32 v39, 0x3fb8aa3b, v39
	v_exp_f32_e32 v36, v36
	v_exp_f32_e32 v37, v37
	v_exp_f32_e32 v38, v38
	v_exp_f32_e32 v39, v39
	v_exp_f32_e32 v40, v40
	v_add_f32_e32 v43, 0, v36
	v_sub_f32_e32 v41, v185, v27
	v_sub_f32_e32 v42, v186, v44
	ds_write_b128 v162, v[36:39]
	v_sub_f32_e32 v36, v187, v45
	v_mul_f32_e32 v41, 0x3fb8aa3b, v41
	v_mul_f32_e32 v42, 0x3fb8aa3b, v42
	v_mul_f32_e32 v36, 0x3fb8aa3b, v36
	v_add_f32_e32 v47, 0, v38
	v_exp_f32_e32 v41, v41
	v_exp_f32_e32 v42, v42
	v_add_f32_e32 v38, v40, v43
	v_exp_f32_e32 v43, v36
	v_sub_f32_e32 v36, v176, v26
	v_mul_f32_e32 v36, 0x3fb8aa3b, v36
	v_sub_f32_e32 v26, v165, v26
	v_exp_f32_e32 v36, v36
	v_mul_f32_e32 v26, 0x3fb8aa3b, v26
	ds_write_b128 v162, v[40:43] offset:1024
	v_exp_f32_e32 v40, v26
	v_add_f32_e32 v46, 0, v37
	v_sub_f32_e32 v26, v178, v44
	v_add_f32_e32 v48, 0, v39
	v_add_f32_e32 v39, v41, v46
	v_add_f32_e32 v41, v36, v38
	v_mul_f32_e32 v26, 0x3fb8aa3b, v26
	v_exp_f32_e32 v38, v26
	v_add_f32_e32 v26, v40, v41
	ds_bpermute_b32 v41, v167, v26
	v_add_f32_e32 v46, v42, v47
	v_add_f32_e32 v47, v43, v48
	v_sub_f32_e32 v37, v177, v27
	v_mul_f32_e32 v37, 0x3fb8aa3b, v37
	s_waitcnt lgkmcnt(0)
	v_add_f32_e32 v26, v26, v41
	ds_bpermute_b32 v43, v168, v26
	v_exp_f32_e32 v37, v37
	v_sub_f32_e32 v27, v169, v27
	v_mul_f32_e32 v27, 0x3fb8aa3b, v27
	v_exp_f32_e32 v41, v27
	s_waitcnt lgkmcnt(0)
	v_add_f32_e32 v26, v26, v43
	ds_bpermute_b32 v27, v170, v26
	v_add_f32_e32 v42, v37, v39
	v_sub_f32_e32 v39, v183, v45
	v_mul_f32_e32 v39, 0x3fb8aa3b, v39
	v_exp_f32_e32 v39, v39
	s_waitcnt lgkmcnt(0)
	v_add_f32_e32 v26, v26, v27
	ds_bpermute_b32 v27, v171, v26
	v_add_f32_e32 v46, v38, v46
	ds_write_b128 v162, v[36:39] offset:2048
	v_sub_f32_e32 v37, v174, v44
	v_mul_f32_e32 v37, 0x3fb8aa3b, v37
	v_add_f32_e32 v36, v41, v42
	v_exp_f32_e32 v42, v37
	v_sub_f32_e32 v37, v175, v45
	v_mul_f32_e32 v37, 0x3fb8aa3b, v37
	s_waitcnt lgkmcnt(1)
	v_add_f32_e32 v26, v26, v27
	v_exp_f32_e32 v43, v37
	ds_bpermute_b32 v27, v172, v26
	v_add_f32_e32 v47, v39, v47
	v_add_f32_e32 v37, v42, v46
	v_add_f32_e32 v38, v43, v47
	ds_bpermute_b32 v39, v167, v36
	s_waitcnt lgkmcnt(1)
	v_add_f32_e32 v66, v26, v27
	ds_bpermute_b32 v26, v167, v37
	ds_bpermute_b32 v27, v167, v38
	ds_bpermute_b32 v67, v173, v66
	s_waitcnt lgkmcnt(3)
	v_add_f32_e32 v36, v36, v39
	ds_bpermute_b32 v39, v168, v36
	s_waitcnt lgkmcnt(3)
	v_add_f32_e32 v26, v37, v26
	s_waitcnt lgkmcnt(2)
	v_add_f32_e32 v27, v38, v27
	ds_bpermute_b32 v37, v168, v26
	ds_bpermute_b32 v38, v168, v27
	s_waitcnt lgkmcnt(2)
	v_add_f32_e32 v36, v36, v39
	ds_bpermute_b32 v39, v170, v36
	ds_write_b128 v162, v[40:43] offset:3072
	s_waitcnt lgkmcnt(3)
	v_add_f32_e32 v26, v26, v37
	s_waitcnt lgkmcnt(2)
	v_add_f32_e32 v27, v27, v38
	ds_bpermute_b32 v37, v170, v26
	ds_bpermute_b32 v38, v170, v27
	s_waitcnt lgkmcnt(3)
	v_add_f32_e32 v36, v36, v39
	ds_bpermute_b32 v39, v171, v36
	s_waitcnt lgkmcnt(2)
	v_add_f32_e32 v26, v26, v37
	s_waitcnt lgkmcnt(1)
	v_add_f32_e32 v27, v27, v38
	ds_bpermute_b32 v37, v171, v26
	ds_bpermute_b32 v38, v171, v27
	s_waitcnt lgkmcnt(2)
	v_add_f32_e32 v36, v36, v39
	ds_bpermute_b32 v39, v172, v36
	s_waitcnt lgkmcnt(2)
	v_add_f32_e32 v26, v26, v37
	s_waitcnt lgkmcnt(1)
	v_add_f32_e32 v27, v27, v38
	ds_bpermute_b32 v37, v172, v26
	ds_bpermute_b32 v38, v172, v27
	s_waitcnt lgkmcnt(2)
	v_add_f32_e32 v68, v36, v39
	ds_bpermute_b32 v69, v173, v68
	s_waitcnt lgkmcnt(2)
	v_add_f32_e32 v70, v26, v37
	s_waitcnt lgkmcnt(1)
	v_add_f32_e32 v72, v27, v38
	ds_bpermute_b32 v71, v173, v70
	ds_bpermute_b32 v73, v173, v72
	v_mov_b32_e32 v36, 0
	v_mov_b32_e32 v37, v36
	v_mov_b32_e32 v38, v36
	v_mov_b32_e32 v39, v36
	v_mov_b32_e32 v40, v36
	v_mov_b32_e32 v41, v36
	v_mov_b32_e32 v42, v36
	v_mov_b32_e32 v43, v36
	v_mov_b32_e32 v44, v36
	v_mov_b32_e32 v45, v36
	v_mov_b32_e32 v46, v36
	v_mov_b32_e32 v47, v36
	v_mov_b32_e32 v48, v36
	v_mov_b32_e32 v49, v36
	v_mov_b32_e32 v50, v36
	v_mov_b32_e32 v51, v36
	v_mov_b32_e32 v52, v36
	v_mov_b32_e32 v53, v36
	v_mov_b32_e32 v54, v36
	v_mov_b32_e32 v55, v36
	v_mov_b32_e32 v56, v36
	v_mov_b32_e32 v57, v36
	v_mov_b32_e32 v58, v36
	v_mov_b32_e32 v59, v36
	v_mov_b32_e32 v60, v36
	v_mov_b32_e32 v61, v36
	v_mov_b32_e32 v62, v36
	v_mov_b32_e32 v63, v36
	v_mov_b32_e32 v224, v36
	v_mov_b32_e32 v225, v36
	v_mov_b32_e32 v226, v36
	v_mov_b32_e32 v227, v36

.LBB0_1239:
	v_lshl_add_u32 v236, v75, 4, v82
	v_mbcnt_lo_u32_b32 v228, -1, 0
	v_mbcnt_hi_u32_b32 v228, -1, v228
	v_and_b32_e32 v228, 3, v228
	v_lshl_add_u32 v236, v228, 2, v236
	ds_read_b32 v220, v236
	ds_read_b32 v221, v236 offset:64
	s_waitcnt vmcnt(15)
	v_cvt_pk_f32_fp8_e32 v[192:193], v3
	v_cvt_pk_f32_fp8_sdwa v[194:195], v3 src0_sel:WORD_1
	s_waitcnt lgkmcnt(1)
	v_cvt_pk_f32_fp8_e32 v[78:79], v2
	v_cvt_pk_f32_fp8_sdwa v[80:81], v2 src0_sel:WORD_1
	s_waitcnt lgkmcnt(0)
	v_mfma_f32_4x4x1_16b_f32 v[36:39], v220, v78, v[36:39]
	v_mfma_f32_4x4x1_16b_f32 v[40:43], v220, v79, v[40:43]
	v_mfma_f32_4x4x1_16b_f32 v[44:47], v220, v80, v[44:47]
	v_mfma_f32_4x4x1_16b_f32 v[48:51], v220, v81, v[48:51]
	v_mfma_f32_4x4x1_16b_f32 v[52:55], v220, v192, v[52:55]
	v_mfma_f32_4x4x1_16b_f32 v[56:59], v220, v193, v[56:59]
	v_mfma_f32_4x4x1_16b_f32 v[60:63], v220, v194, v[60:63]
	s_waitcnt vmcnt(14)
	v_cvt_pk_f32_fp8_e32 v[78:79], v4
	v_cvt_pk_f32_fp8_sdwa v[80:81], v4 src0_sel:WORD_1
	v_cvt_pk_f32_fp8_e32 v[188:189], v5
	v_cvt_pk_f32_fp8_sdwa v[190:191], v5 src0_sel:WORD_1
	v_mfma_f32_4x4x1_16b_f32 v[36:39], v221, v78, v[36:39]
	v_mfma_f32_4x4x1_16b_f32 v[52:55], v221, v188, v[52:55]
	v_mfma_f32_4x4x1_16b_f32 v[224:227], v220, v195, v[224:227]
	v_mfma_f32_4x4x1_16b_f32 v[40:43], v221, v79, v[40:43]
	v_mfma_f32_4x4x1_16b_f32 v[44:47], v221, v80, v[44:47]
	v_mfma_f32_4x4x1_16b_f32 v[48:51], v221, v81, v[48:51]
	ds_read_b32 v222, v236 offset:128
	v_mfma_f32_4x4x1_16b_f32 v[56:59], v221, v189, v[56:59]
	v_mfma_f32_4x4x1_16b_f32 v[60:63], v221, v190, v[60:63]
	v_mfma_f32_4x4x1_16b_f32 v[224:227], v221, v191, v[224:227]
	ds_read_b32 v223, v236 offset:192
	s_waitcnt vmcnt(13)
	v_cvt_pk_f32_fp8_e32 v[192:193], v7
	v_cvt_pk_f32_fp8_sdwa v[194:195], v7 src0_sel:WORD_1
	s_waitcnt lgkmcnt(1)
	v_cvt_pk_f32_fp8_e32 v[78:79], v6
	v_cvt_pk_f32_fp8_sdwa v[80:81], v6 src0_sel:WORD_1
	s_nop 0
	v_mfma_f32_4x4x1_16b_f32 v[36:39], v222, v78, v[36:39]
	v_mfma_f32_4x4x1_16b_f32 v[40:43], v222, v79, v[40:43]
	v_mfma_f32_4x4x1_16b_f32 v[44:47], v222, v80, v[44:47]
	v_mfma_f32_4x4x1_16b_f32 v[48:51], v222, v81, v[48:51]
	v_mfma_f32_4x4x1_16b_f32 v[52:55], v222, v192, v[52:55]
	v_mfma_f32_4x4x1_16b_f32 v[56:59], v222, v193, v[56:59]
	v_mfma_f32_4x4x1_16b_f32 v[60:63], v222, v194, v[60:63]
	v_mfma_f32_4x4x1_16b_f32 v[224:227], v222, v195, v[224:227]
	s_waitcnt vmcnt(12)
	v_cvt_pk_f32_fp8_e32 v[78:79], v8
	v_cvt_pk_f32_fp8_sdwa v[80:81], v8 src0_sel:WORD_1
	s_waitcnt lgkmcnt(0)
	v_cvt_pk_f32_fp8_e32 v[188:189], v9
	v_cvt_pk_f32_fp8_sdwa v[190:191], v9 src0_sel:WORD_1
	v_mfma_f32_4x4x1_16b_f32 v[36:39], v223, v78, v[36:39]
	v_mfma_f32_4x4x1_16b_f32 v[40:43], v223, v79, v[40:43]
	v_mfma_f32_4x4x1_16b_f32 v[44:47], v223, v80, v[44:47]
	v_mfma_f32_4x4x1_16b_f32 v[48:51], v223, v81, v[48:51]
	v_mfma_f32_4x4x1_16b_f32 v[52:55], v223, v188, v[52:55]
	v_mfma_f32_4x4x1_16b_f32 v[56:59], v223, v189, v[56:59]
	v_mfma_f32_4x4x1_16b_f32 v[60:63], v223, v190, v[60:63]
	v_mfma_f32_4x4x1_16b_f32 v[224:227], v223, v191, v[224:227]
	ds_read_b32 v220, v236 offset:256
	ds_read_b32 v221, v236 offset:320
	s_waitcnt vmcnt(11)
	v_cvt_pk_f32_fp8_e32 v[192:193], v11
	v_cvt_pk_f32_fp8_sdwa v[194:195], v11 src0_sel:WORD_1
	s_waitcnt lgkmcnt(1)
	v_cvt_pk_f32_fp8_e32 v[78:79], v10
	v_cvt_pk_f32_fp8_sdwa v[80:81], v10 src0_sel:WORD_1
	s_waitcnt lgkmcnt(0)
	v_mfma_f32_4x4x1_16b_f32 v[36:39], v220, v78, v[36:39]
	v_mfma_f32_4x4x1_16b_f32 v[40:43], v220, v79, v[40:43]
	v_mfma_f32_4x4x1_16b_f32 v[44:47], v220, v80, v[44:47]
	v_mfma_f32_4x4x1_16b_f32 v[48:51], v220, v81, v[48:51]
	v_mfma_f32_4x4x1_16b_f32 v[52:55], v220, v192, v[52:55]
	v_mfma_f32_4x4x1_16b_f32 v[56:59], v220, v193, v[56:59]
	v_mfma_f32_4x4x1_16b_f32 v[60:63], v220, v194, v[60:63]
	s_waitcnt vmcnt(10)
	v_cvt_pk_f32_fp8_e32 v[78:79], v12
	v_cvt_pk_f32_fp8_sdwa v[80:81], v12 src0_sel:WORD_1
	v_cvt_pk_f32_fp8_e32 v[188:189], v13
	v_cvt_pk_f32_fp8_sdwa v[190:191], v13 src0_sel:WORD_1
	v_mfma_f32_4x4x1_16b_f32 v[36:39], v221, v78, v[36:39]
	v_mfma_f32_4x4x1_16b_f32 v[52:55], v221, v188, v[52:55]
	v_mfma_f32_4x4x1_16b_f32 v[224:227], v220, v195, v[224:227]
	v_mfma_f32_4x4x1_16b_f32 v[40:43], v221, v79, v[40:43]
	v_mfma_f32_4x4x1_16b_f32 v[44:47], v221, v80, v[44:47]
	v_mfma_f32_4x4x1_16b_f32 v[48:51], v221, v81, v[48:51]
	ds_read_b32 v222, v236 offset:384
	v_mfma_f32_4x4x1_16b_f32 v[56:59], v221, v189, v[56:59]
	v_mfma_f32_4x4x1_16b_f32 v[60:63], v221, v190, v[60:63]
	v_mfma_f32_4x4x1_16b_f32 v[224:227], v221, v191, v[224:227]
	ds_read_b32 v223, v236 offset:448
	s_waitcnt vmcnt(9)
	v_cvt_pk_f32_fp8_e32 v[192:193], v15
	v_cvt_pk_f32_fp8_sdwa v[194:195], v15 src0_sel:WORD_1
	s_waitcnt lgkmcnt(1)
	v_cvt_pk_f32_fp8_e32 v[78:79], v14
	v_cvt_pk_f32_fp8_sdwa v[80:81], v14 src0_sel:WORD_1
	s_nop 0
	v_mfma_f32_4x4x1_16b_f32 v[36:39], v222, v78, v[36:39]
	v_mfma_f32_4x4x1_16b_f32 v[40:43], v222, v79, v[40:43]
	v_mfma_f32_4x4x1_16b_f32 v[44:47], v222, v80, v[44:47]
	v_mfma_f32_4x4x1_16b_f32 v[48:51], v222, v81, v[48:51]
	v_mfma_f32_4x4x1_16b_f32 v[52:55], v222, v192, v[52:55]
	v_mfma_f32_4x4x1_16b_f32 v[56:59], v222, v193, v[56:59]
	v_mfma_f32_4x4x1_16b_f32 v[60:63], v222, v194, v[60:63]
	v_mfma_f32_4x4x1_16b_f32 v[224:227], v222, v195, v[224:227]
	s_waitcnt vmcnt(8)
	v_cvt_pk_f32_fp8_e32 v[78:79], v16
	v_cvt_pk_f32_fp8_sdwa v[80:81], v16 src0_sel:WORD_1
	s_waitcnt lgkmcnt(0)
	v_cvt_pk_f32_fp8_e32 v[188:189], v17
	v_cvt_pk_f32_fp8_sdwa v[190:191], v17 src0_sel:WORD_1
	v_mfma_f32_4x4x1_16b_f32 v[36:39], v223, v78, v[36:39]
	v_mfma_f32_4x4x1_16b_f32 v[40:43], v223, v79, v[40:43]
	v_mfma_f32_4x4x1_16b_f32 v[44:47], v223, v80, v[44:47]
	v_mfma_f32_4x4x1_16b_f32 v[48:51], v223, v81, v[48:51]
	v_mfma_f32_4x4x1_16b_f32 v[52:55], v223, v188, v[52:55]
	v_mfma_f32_4x4x1_16b_f32 v[56:59], v223, v189, v[56:59]
	v_mfma_f32_4x4x1_16b_f32 v[60:63], v223, v190, v[60:63]
	v_mfma_f32_4x4x1_16b_f32 v[224:227], v223, v191, v[224:227]
	ds_read_b32 v220, v236 offset:512
	ds_read_b32 v221, v236 offset:576
	s_waitcnt vmcnt(7)
	v_cvt_pk_f32_fp8_e32 v[192:193], v19
	v_cvt_pk_f32_fp8_sdwa v[194:195], v19 src0_sel:WORD_1
	s_waitcnt lgkmcnt(1)
	v_cvt_pk_f32_fp8_e32 v[78:79], v18
	v_cvt_pk_f32_fp8_sdwa v[80:81], v18 src0_sel:WORD_1
	s_waitcnt lgkmcnt(0)
	v_mfma_f32_4x4x1_16b_f32 v[36:39], v220, v78, v[36:39]
	v_mfma_f32_4x4x1_16b_f32 v[40:43], v220, v79, v[40:43]
	v_mfma_f32_4x4x1_16b_f32 v[44:47], v220, v80, v[44:47]
	v_mfma_f32_4x4x1_16b_f32 v[48:51], v220, v81, v[48:51]
	v_mfma_f32_4x4x1_16b_f32 v[52:55], v220, v192, v[52:55]
	v_mfma_f32_4x4x1_16b_f32 v[56:59], v220, v193, v[56:59]
	v_mfma_f32_4x4x1_16b_f32 v[60:63], v220, v194, v[60:63]
	s_waitcnt vmcnt(6)
	v_cvt_pk_f32_fp8_e32 v[78:79], v20
	v_cvt_pk_f32_fp8_sdwa v[80:81], v20 src0_sel:WORD_1
	v_cvt_pk_f32_fp8_e32 v[188:189], v21
	v_cvt_pk_f32_fp8_sdwa v[190:191], v21 src0_sel:WORD_1
	v_mfma_f32_4x4x1_16b_f32 v[36:39], v221, v78, v[36:39]
	v_mfma_f32_4x4x1_16b_f32 v[52:55], v221, v188, v[52:55]
	v_mfma_f32_4x4x1_16b_f32 v[224:227], v220, v195, v[224:227]
	v_mfma_f32_4x4x1_16b_f32 v[40:43], v221, v79, v[40:43]
	v_mfma_f32_4x4x1_16b_f32 v[44:47], v221, v80, v[44:47]
	v_mfma_f32_4x4x1_16b_f32 v[48:51], v221, v81, v[48:51]
	ds_read_b32 v222, v236 offset:640
	v_mfma_f32_4x4x1_16b_f32 v[56:59], v221, v189, v[56:59]
	v_mfma_f32_4x4x1_16b_f32 v[60:63], v221, v190, v[60:63]
	v_mfma_f32_4x4x1_16b_f32 v[224:227], v221, v191, v[224:227]
	ds_read_b32 v223, v236 offset:704
	s_waitcnt vmcnt(5)
	v_cvt_pk_f32_fp8_e32 v[192:193], v23
	v_cvt_pk_f32_fp8_sdwa v[194:195], v23 src0_sel:WORD_1
	s_waitcnt lgkmcnt(1)
	v_cvt_pk_f32_fp8_e32 v[78:79], v22
	v_cvt_pk_f32_fp8_sdwa v[80:81], v22 src0_sel:WORD_1
	s_nop 0
	v_mfma_f32_4x4x1_16b_f32 v[36:39], v222, v78, v[36:39]
	v_mfma_f32_4x4x1_16b_f32 v[40:43], v222, v79, v[40:43]
	v_mfma_f32_4x4x1_16b_f32 v[44:47], v222, v80, v[44:47]
	v_mfma_f32_4x4x1_16b_f32 v[48:51], v222, v81, v[48:51]
	v_mfma_f32_4x4x1_16b_f32 v[52:55], v222, v192, v[52:55]
	v_mfma_f32_4x4x1_16b_f32 v[56:59], v222, v193, v[56:59]
	v_mfma_f32_4x4x1_16b_f32 v[60:63], v222, v194, v[60:63]
	v_mfma_f32_4x4x1_16b_f32 v[224:227], v222, v195, v[224:227]
	s_waitcnt vmcnt(4)
	v_cvt_pk_f32_fp8_e32 v[78:79], v24
	v_cvt_pk_f32_fp8_sdwa v[80:81], v24 src0_sel:WORD_1
	s_waitcnt lgkmcnt(0)
	v_cvt_pk_f32_fp8_e32 v[188:189], v25
	v_cvt_pk_f32_fp8_sdwa v[190:191], v25 src0_sel:WORD_1
	v_mfma_f32_4x4x1_16b_f32 v[36:39], v223, v78, v[36:39]
	v_mfma_f32_4x4x1_16b_f32 v[40:43], v223, v79, v[40:43]
	v_mfma_f32_4x4x1_16b_f32 v[44:47], v223, v80, v[44:47]
	v_mfma_f32_4x4x1_16b_f32 v[48:51], v223, v81, v[48:51]
	v_mfma_f32_4x4x1_16b_f32 v[52:55], v223, v188, v[52:55]
	v_mfma_f32_4x4x1_16b_f32 v[56:59], v223, v189, v[56:59]
	v_mfma_f32_4x4x1_16b_f32 v[60:63], v223, v190, v[60:63]
	v_mfma_f32_4x4x1_16b_f32 v[224:227], v223, v191, v[224:227]
	ds_read_b32 v220, v236 offset:768
	ds_read_b32 v221, v236 offset:832
	s_waitcnt vmcnt(3)
	v_cvt_pk_f32_fp8_e32 v[192:193], v29
	v_cvt_pk_f32_fp8_sdwa v[194:195], v29 src0_sel:WORD_1
	s_waitcnt lgkmcnt(1)
	v_cvt_pk_f32_fp8_e32 v[78:79], v28
	v_cvt_pk_f32_fp8_sdwa v[80:81], v28 src0_sel:WORD_1
	s_waitcnt lgkmcnt(0)
	v_mfma_f32_4x4x1_16b_f32 v[36:39], v220, v78, v[36:39]
	v_mfma_f32_4x4x1_16b_f32 v[40:43], v220, v79, v[40:43]
	v_mfma_f32_4x4x1_16b_f32 v[44:47], v220, v80, v[44:47]
	v_mfma_f32_4x4x1_16b_f32 v[48:51], v220, v81, v[48:51]
	v_mfma_f32_4x4x1_16b_f32 v[52:55], v220, v192, v[52:55]
	v_mfma_f32_4x4x1_16b_f32 v[56:59], v220, v193, v[56:59]
	v_mfma_f32_4x4x1_16b_f32 v[60:63], v220, v194, v[60:63]
	s_waitcnt vmcnt(2)
	v_cvt_pk_f32_fp8_e32 v[78:79], v30
	v_cvt_pk_f32_fp8_sdwa v[80:81], v30 src0_sel:WORD_1
	v_cvt_pk_f32_fp8_e32 v[188:189], v31
	v_cvt_pk_f32_fp8_sdwa v[190:191], v31 src0_sel:WORD_1
	v_mfma_f32_4x4x1_16b_f32 v[36:39], v221, v78, v[36:39]
	v_mfma_f32_4x4x1_16b_f32 v[52:55], v221, v188, v[52:55]
	v_mfma_f32_4x4x1_16b_f32 v[224:227], v220, v195, v[224:227]
	v_mfma_f32_4x4x1_16b_f32 v[40:43], v221, v79, v[40:43]
	v_mfma_f32_4x4x1_16b_f32 v[44:47], v221, v80, v[44:47]
	v_mfma_f32_4x4x1_16b_f32 v[48:51], v221, v81, v[48:51]
	ds_read_b32 v222, v236 offset:896
	v_mfma_f32_4x4x1_16b_f32 v[56:59], v221, v189, v[56:59]
	v_mfma_f32_4x4x1_16b_f32 v[60:63], v221, v190, v[60:63]
	v_mfma_f32_4x4x1_16b_f32 v[224:227], v221, v191, v[224:227]
	ds_read_b32 v223, v236 offset:960
	s_waitcnt vmcnt(1)
	v_cvt_pk_f32_fp8_e32 v[192:193], v33
	v_cvt_pk_f32_fp8_sdwa v[194:195], v33 src0_sel:WORD_1
	s_waitcnt lgkmcnt(1)
	v_cvt_pk_f32_fp8_e32 v[78:79], v32
	v_cvt_pk_f32_fp8_sdwa v[80:81], v32 src0_sel:WORD_1
	s_nop 0
	v_mfma_f32_4x4x1_16b_f32 v[36:39], v222, v78, v[36:39]
	v_mfma_f32_4x4x1_16b_f32 v[40:43], v222, v79, v[40:43]
	v_mfma_f32_4x4x1_16b_f32 v[44:47], v222, v80, v[44:47]
	v_mfma_f32_4x4x1_16b_f32 v[48:51], v222, v81, v[48:51]
	v_mfma_f32_4x4x1_16b_f32 v[52:55], v222, v192, v[52:55]
	v_mfma_f32_4x4x1_16b_f32 v[56:59], v222, v193, v[56:59]
	v_mfma_f32_4x4x1_16b_f32 v[60:63], v222, v194, v[60:63]
	v_mfma_f32_4x4x1_16b_f32 v[224:227], v222, v195, v[224:227]
	s_waitcnt vmcnt(0)
	v_cvt_pk_f32_fp8_e32 v[78:79], v34
	v_cvt_pk_f32_fp8_sdwa v[80:81], v34 src0_sel:WORD_1
	s_waitcnt lgkmcnt(0)
	v_cvt_pk_f32_fp8_e32 v[188:189], v35
	v_cvt_pk_f32_fp8_sdwa v[190:191], v35 src0_sel:WORD_1
	v_mfma_f32_4x4x1_16b_f32 v[36:39], v223, v78, v[36:39]
	v_mfma_f32_4x4x1_16b_f32 v[40:43], v223, v79, v[40:43]
	v_mfma_f32_4x4x1_16b_f32 v[44:47], v223, v80, v[44:47]
	v_mfma_f32_4x4x1_16b_f32 v[48:51], v223, v81, v[48:51]
	v_mfma_f32_4x4x1_16b_f32 v[52:55], v223, v188, v[52:55]
	v_mfma_f32_4x4x1_16b_f32 v[56:59], v223, v189, v[56:59]
	v_mfma_f32_4x4x1_16b_f32 v[60:63], v223, v190, v[60:63]
	v_mfma_f32_4x4x1_16b_f32 v[224:227], v223, v191, v[224:227]
	s_andn2_b64 vcc, exec, s[14:15]
	s_cbranch_vccnz .LBB0_1243
	s_cmp_ge_u32 s16, s3
	s_cbranch_scc1 .LBB0_1242
	v_lshl_add_u32 v237, v74, 1, v84
	ds_read_u16 v2, v237 offset:33024
	ds_read_u16 v10, v237 offset:33032
	ds_read_u16 v11, v237 offset:33040
	ds_read_u16 v12, v237 offset:33048
	ds_read_u16 v13, v237 offset:33056
	ds_read_u16 v14, v237 offset:33064
	ds_read_u16 v15, v237 offset:33072
	ds_read_u16 v16, v237 offset:33080
	s_waitcnt lgkmcnt(7)
	v_lshlrev_b32_e32 v86, 9, v2
	v_lshl_add_u64 v[2:3], v[118:119], 0, v[86:87]
	s_waitcnt lgkmcnt(6)
	v_lshlrev_b32_e32 v86, 9, v10
	v_lshl_add_u64 v[4:5], v[118:119], 0, v[86:87]
	s_waitcnt lgkmcnt(5)
	v_lshlrev_b32_e32 v86, 9, v11
	v_lshl_add_u64 v[6:7], v[118:119], 0, v[86:87]
	s_waitcnt lgkmcnt(4)
	v_lshlrev_b32_e32 v86, 9, v12
	v_lshl_add_u64 v[8:9], v[118:119], 0, v[86:87]
	s_waitcnt lgkmcnt(3)
	v_lshlrev_b32_e32 v86, 9, v13
	v_lshl_add_u64 v[10:11], v[118:119], 0, v[86:87]
	s_waitcnt lgkmcnt(2)
	v_lshlrev_b32_e32 v86, 9, v14
	v_lshl_add_u64 v[12:13], v[118:119], 0, v[86:87]
	s_waitcnt lgkmcnt(1)
	v_lshlrev_b32_e32 v86, 9, v15
	v_lshl_add_u64 v[14:15], v[118:119], 0, v[86:87]
	s_waitcnt lgkmcnt(0)
	v_lshlrev_b32_e32 v86, 9, v16
	v_lshl_add_u64 v[16:17], v[118:119], 0, v[86:87]
	global_load_dwordx2 v[2:3], v[2:3], off offset:128
	s_nop 0
	global_load_dwordx2 v[4:5], v[4:5], off offset:128
	s_nop 0
	global_load_dwordx2 v[6:7], v[6:7], off offset:128
	s_nop 0
	global_load_dwordx2 v[8:9], v[8:9], off offset:128
	s_nop 0
	global_load_dwordx2 v[10:11], v[10:11], off offset:128
	s_nop 0
	global_load_dwordx2 v[12:13], v[12:13], off offset:128
	s_nop 0
	global_load_dwordx2 v[14:15], v[14:15], off offset:128
	s_nop 0
	global_load_dwordx2 v[16:17], v[16:17], off offset:128
	ds_read_u16 v18, v237 offset:33088
	ds_read_u16 v28, v237 offset:33096
	ds_read_u16 v29, v237 offset:33104
	ds_read_u16 v30, v237 offset:33112
	ds_read_u16 v31, v237 offset:33120
	ds_read_u16 v32, v237 offset:33128
	ds_read_u16 v33, v237 offset:33136
	ds_read_u16 v34, v237 offset:33144
	s_waitcnt lgkmcnt(7)
	v_lshlrev_b32_e32 v86, 9, v18
	v_lshl_add_u64 v[18:19], v[118:119], 0, v[86:87]
	s_waitcnt lgkmcnt(6)
	v_lshlrev_b32_e32 v86, 9, v28
	v_lshl_add_u64 v[20:21], v[118:119], 0, v[86:87]
	s_waitcnt lgkmcnt(5)
	v_lshlrev_b32_e32 v86, 9, v29
	v_lshl_add_u64 v[22:23], v[118:119], 0, v[86:87]
	s_waitcnt lgkmcnt(4)
	v_lshlrev_b32_e32 v86, 9, v30
	v_lshl_add_u64 v[24:25], v[118:119], 0, v[86:87]
	s_waitcnt lgkmcnt(3)
	v_lshlrev_b32_e32 v86, 9, v31
	v_lshl_add_u64 v[28:29], v[118:119], 0, v[86:87]
	s_waitcnt lgkmcnt(2)
	v_lshlrev_b32_e32 v86, 9, v32
	v_lshl_add_u64 v[30:31], v[118:119], 0, v[86:87]
	s_waitcnt lgkmcnt(1)
	v_lshlrev_b32_e32 v86, 9, v33
	v_lshl_add_u64 v[32:33], v[118:119], 0, v[86:87]
	s_waitcnt lgkmcnt(0)
	v_lshlrev_b32_e32 v86, 9, v34
	v_lshl_add_u64 v[34:35], v[118:119], 0, v[86:87]
	global_load_dwordx2 v[18:19], v[18:19], off offset:128
	s_nop 0
	global_load_dwordx2 v[20:21], v[20:21], off offset:128
	s_nop 0
	global_load_dwordx2 v[22:23], v[22:23], off offset:128
	s_nop 0
	global_load_dwordx2 v[24:25], v[24:25], off offset:128
	s_nop 0
	global_load_dwordx2 v[28:29], v[28:29], off offset:128
	s_nop 0
	global_load_dwordx2 v[30:31], v[30:31], off offset:128
	s_nop 0
	global_load_dwordx2 v[32:33], v[32:33], off offset:128
	s_nop 0
	global_load_dwordx2 v[34:35], v[34:35], off offset:128
.LBB0_1242:
	ds_read_b32 v220, v236 offset:1024
	ds_read_b32 v221, v236 offset:1088
	v_cvt_pk_f32_fp8_e32 v[76:77], v104
	v_cvt_pk_f32_fp8_sdwa v[192:193], v105 src0_sel:WORD_1
	s_waitcnt lgkmcnt(1)
	v_cvt_pk_f32_fp8_e32 v[80:81], v105
	s_nop 1
	v_mfma_f32_4x4x1_16b_f32 v[52:55], v220, v80, v[52:55]
	v_mfma_f32_4x4x1_16b_f32 v[56:59], v220, v81, v[56:59]
	v_cvt_pk_f32_fp8_e32 v[80:81], v103
	v_cvt_pk_f32_fp8_sdwa v[78:79], v104 src0_sel:WORD_1
	v_mfma_f32_4x4x1_16b_f32 v[36:39], v220, v76, v[36:39]
	v_mfma_f32_4x4x1_16b_f32 v[40:43], v220, v77, v[40:43]
	v_mfma_f32_4x4x1_16b_f32 v[60:63], v220, v192, v[60:63]
	s_waitcnt lgkmcnt(0)
	v_cvt_pk_f32_fp8_e32 v[76:77], v102
	v_mfma_f32_4x4x1_16b_f32 v[52:55], v221, v80, v[52:55]
	v_mfma_f32_4x4x1_16b_f32 v[44:47], v220, v78, v[44:47]
	v_mfma_f32_4x4x1_16b_f32 v[48:51], v220, v79, v[48:51]
	v_cvt_pk_f32_fp8_sdwa v[78:79], v102 src0_sel:WORD_1
	v_cvt_pk_f32_fp8_sdwa v[188:189], v103 src0_sel:WORD_1
	v_mfma_f32_4x4x1_16b_f32 v[36:39], v221, v76, v[36:39]
	v_mfma_f32_4x4x1_16b_f32 v[56:59], v221, v81, v[56:59]
	v_mfma_f32_4x4x1_16b_f32 v[224:227], v220, v193, v[224:227]
	v_mfma_f32_4x4x1_16b_f32 v[40:43], v221, v77, v[40:43]
	v_mfma_f32_4x4x1_16b_f32 v[44:47], v221, v78, v[44:47]
	v_mfma_f32_4x4x1_16b_f32 v[48:51], v221, v79, v[48:51]
	ds_read_b32 v222, v236 offset:1152
	v_mfma_f32_4x4x1_16b_f32 v[60:63], v221, v188, v[60:63]
	v_mfma_f32_4x4x1_16b_f32 v[224:227], v221, v189, v[224:227]
	ds_read_b32 v223, v236 offset:1216
	v_cvt_pk_f32_fp8_e32 v[80:81], v101
	v_cvt_pk_f32_fp8_sdwa v[192:193], v101 src0_sel:WORD_1
	s_waitcnt lgkmcnt(1)
	v_cvt_pk_f32_fp8_e32 v[76:77], v100
	v_cvt_pk_f32_fp8_sdwa v[78:79], v100 src0_sel:WORD_1
	s_nop 0
	v_mfma_f32_4x4x1_16b_f32 v[36:39], v222, v76, v[36:39]
	v_mfma_f32_4x4x1_16b_f32 v[40:43], v222, v77, v[40:43]
	v_mfma_f32_4x4x1_16b_f32 v[44:47], v222, v78, v[44:47]
	v_mfma_f32_4x4x1_16b_f32 v[48:51], v222, v79, v[48:51]
	v_mfma_f32_4x4x1_16b_f32 v[52:55], v222, v80, v[52:55]
	v_mfma_f32_4x4x1_16b_f32 v[56:59], v222, v81, v[56:59]
	v_mfma_f32_4x4x1_16b_f32 v[60:63], v222, v192, v[60:63]
	v_mfma_f32_4x4x1_16b_f32 v[224:227], v222, v193, v[224:227]
	v_cvt_pk_f32_fp8_e32 v[76:77], v98
	v_cvt_pk_f32_fp8_sdwa v[78:79], v98 src0_sel:WORD_1
	s_waitcnt lgkmcnt(0)
	v_cvt_pk_f32_fp8_e32 v[80:81], v99
	v_cvt_pk_f32_fp8_sdwa v[188:189], v99 src0_sel:WORD_1
	v_mfma_f32_4x4x1_16b_f32 v[36:39], v223, v76, v[36:39]
	v_mfma_f32_4x4x1_16b_f32 v[40:43], v223, v77, v[40:43]
	v_mfma_f32_4x4x1_16b_f32 v[44:47], v223, v78, v[44:47]
	v_mfma_f32_4x4x1_16b_f32 v[48:51], v223, v79, v[48:51]
	v_mfma_f32_4x4x1_16b_f32 v[52:55], v223, v80, v[52:55]
	v_mfma_f32_4x4x1_16b_f32 v[56:59], v223, v81, v[56:59]
	v_mfma_f32_4x4x1_16b_f32 v[60:63], v223, v188, v[60:63]
	v_mfma_f32_4x4x1_16b_f32 v[224:227], v223, v189, v[224:227]
	ds_read_b32 v220, v236 offset:1280
	ds_read_b32 v221, v236 offset:1344
	v_cvt_pk_f32_fp8_e32 v[80:81], v113
	v_cvt_pk_f32_fp8_sdwa v[192:193], v113 src0_sel:WORD_1
	s_waitcnt lgkmcnt(1)
	v_cvt_pk_f32_fp8_e32 v[76:77], v112
	v_mfma_f32_4x4x1_16b_f32 v[52:55], v220, v80, v[52:55]
	v_mfma_f32_4x4x1_16b_f32 v[56:59], v220, v81, v[56:59]
	v_cvt_pk_f32_fp8_e32 v[80:81], v111
	v_cvt_pk_f32_fp8_sdwa v[78:79], v112 src0_sel:WORD_1
	v_mfma_f32_4x4x1_16b_f32 v[36:39], v220, v76, v[36:39]
	v_mfma_f32_4x4x1_16b_f32 v[40:43], v220, v77, v[40:43]
	v_mfma_f32_4x4x1_16b_f32 v[60:63], v220, v192, v[60:63]
	s_waitcnt lgkmcnt(0)
	v_cvt_pk_f32_fp8_e32 v[76:77], v110
	v_mfma_f32_4x4x1_16b_f32 v[52:55], v221, v80, v[52:55]
	v_mfma_f32_4x4x1_16b_f32 v[44:47], v220, v78, v[44:47]
	v_mfma_f32_4x4x1_16b_f32 v[48:51], v220, v79, v[48:51]
	v_cvt_pk_f32_fp8_sdwa v[78:79], v110 src0_sel:WORD_1
	v_cvt_pk_f32_fp8_sdwa v[188:189], v111 src0_sel:WORD_1
	v_mfma_f32_4x4x1_16b_f32 v[36:39], v221, v76, v[36:39]
	v_mfma_f32_4x4x1_16b_f32 v[56:59], v221, v81, v[56:59]
	v_mfma_f32_4x4x1_16b_f32 v[224:227], v220, v193, v[224:227]
	v_mfma_f32_4x4x1_16b_f32 v[40:43], v221, v77, v[40:43]
	v_mfma_f32_4x4x1_16b_f32 v[44:47], v221, v78, v[44:47]
	v_mfma_f32_4x4x1_16b_f32 v[48:51], v221, v79, v[48:51]
	ds_read_b32 v222, v236 offset:1408
	v_mfma_f32_4x4x1_16b_f32 v[60:63], v221, v188, v[60:63]
	v_mfma_f32_4x4x1_16b_f32 v[224:227], v221, v189, v[224:227]
	ds_read_b32 v223, v236 offset:1472
	v_cvt_pk_f32_fp8_e32 v[80:81], v109
	v_cvt_pk_f32_fp8_sdwa v[192:193], v109 src0_sel:WORD_1
	s_waitcnt lgkmcnt(1)
	v_cvt_pk_f32_fp8_e32 v[76:77], v108
	v_cvt_pk_f32_fp8_sdwa v[78:79], v108 src0_sel:WORD_1
	s_nop 0
	v_mfma_f32_4x4x1_16b_f32 v[36:39], v222, v76, v[36:39]
	v_mfma_f32_4x4x1_16b_f32 v[40:43], v222, v77, v[40:43]
	v_mfma_f32_4x4x1_16b_f32 v[44:47], v222, v78, v[44:47]
	v_mfma_f32_4x4x1_16b_f32 v[48:51], v222, v79, v[48:51]
	v_mfma_f32_4x4x1_16b_f32 v[52:55], v222, v80, v[52:55]
	v_mfma_f32_4x4x1_16b_f32 v[56:59], v222, v81, v[56:59]
	v_mfma_f32_4x4x1_16b_f32 v[60:63], v222, v192, v[60:63]
	v_mfma_f32_4x4x1_16b_f32 v[224:227], v222, v193, v[224:227]
	v_cvt_pk_f32_fp8_e32 v[76:77], v106
	v_cvt_pk_f32_fp8_sdwa v[78:79], v106 src0_sel:WORD_1
	s_waitcnt lgkmcnt(0)
	v_cvt_pk_f32_fp8_e32 v[80:81], v107
	v_cvt_pk_f32_fp8_sdwa v[188:189], v107 src0_sel:WORD_1
	v_mfma_f32_4x4x1_16b_f32 v[36:39], v223, v76, v[36:39]
	v_mfma_f32_4x4x1_16b_f32 v[40:43], v223, v77, v[40:43]
	v_mfma_f32_4x4x1_16b_f32 v[44:47], v223, v78, v[44:47]
	v_mfma_f32_4x4x1_16b_f32 v[48:51], v223, v79, v[48:51]
	v_mfma_f32_4x4x1_16b_f32 v[52:55], v223, v80, v[52:55]
	v_mfma_f32_4x4x1_16b_f32 v[56:59], v223, v81, v[56:59]
	v_mfma_f32_4x4x1_16b_f32 v[60:63], v223, v188, v[60:63]
	v_mfma_f32_4x4x1_16b_f32 v[224:227], v223, v189, v[224:227]
	ds_read_b32 v220, v236 offset:1536
	ds_read_b32 v221, v236 offset:1600
	v_cvt_pk_f32_fp8_e32 v[80:81], v129
	v_cvt_pk_f32_fp8_sdwa v[192:193], v129 src0_sel:WORD_1
	s_waitcnt lgkmcnt(1)
	v_cvt_pk_f32_fp8_e32 v[76:77], v128
	v_mfma_f32_4x4x1_16b_f32 v[52:55], v220, v80, v[52:55]
	v_mfma_f32_4x4x1_16b_f32 v[56:59], v220, v81, v[56:59]
	v_cvt_pk_f32_fp8_e32 v[80:81], v127
	v_cvt_pk_f32_fp8_sdwa v[78:79], v128 src0_sel:WORD_1
	v_mfma_f32_4x4x1_16b_f32 v[36:39], v220, v76, v[36:39]
	v_mfma_f32_4x4x1_16b_f32 v[40:43], v220, v77, v[40:43]
	v_mfma_f32_4x4x1_16b_f32 v[60:63], v220, v192, v[60:63]
	s_waitcnt lgkmcnt(0)
	v_cvt_pk_f32_fp8_e32 v[76:77], v126
	v_mfma_f32_4x4x1_16b_f32 v[52:55], v221, v80, v[52:55]
	v_mfma_f32_4x4x1_16b_f32 v[44:47], v220, v78, v[44:47]
	v_mfma_f32_4x4x1_16b_f32 v[48:51], v220, v79, v[48:51]
	v_cvt_pk_f32_fp8_sdwa v[78:79], v126 src0_sel:WORD_1
	v_cvt_pk_f32_fp8_sdwa v[188:189], v127 src0_sel:WORD_1
	v_mfma_f32_4x4x1_16b_f32 v[36:39], v221, v76, v[36:39]
	v_mfma_f32_4x4x1_16b_f32 v[56:59], v221, v81, v[56:59]
	v_mfma_f32_4x4x1_16b_f32 v[224:227], v220, v193, v[224:227]
	v_mfma_f32_4x4x1_16b_f32 v[40:43], v221, v77, v[40:43]
	v_mfma_f32_4x4x1_16b_f32 v[44:47], v221, v78, v[44:47]
	v_mfma_f32_4x4x1_16b_f32 v[48:51], v221, v79, v[48:51]
	ds_read_b32 v222, v236 offset:1664
	v_mfma_f32_4x4x1_16b_f32 v[60:63], v221, v188, v[60:63]
	v_mfma_f32_4x4x1_16b_f32 v[224:227], v221, v189, v[224:227]
	ds_read_b32 v223, v236 offset:1728
	v_cvt_pk_f32_fp8_e32 v[80:81], v125
	v_cvt_pk_f32_fp8_sdwa v[192:193], v125 src0_sel:WORD_1
	s_waitcnt lgkmcnt(1)
	v_cvt_pk_f32_fp8_e32 v[76:77], v124
	v_cvt_pk_f32_fp8_sdwa v[78:79], v124 src0_sel:WORD_1
	s_nop 0
	v_mfma_f32_4x4x1_16b_f32 v[36:39], v222, v76, v[36:39]
	v_mfma_f32_4x4x1_16b_f32 v[40:43], v222, v77, v[40:43]
	v_mfma_f32_4x4x1_16b_f32 v[44:47], v222, v78, v[44:47]
	v_mfma_f32_4x4x1_16b_f32 v[48:51], v222, v79, v[48:51]
	v_mfma_f32_4x4x1_16b_f32 v[52:55], v222, v80, v[52:55]
	v_mfma_f32_4x4x1_16b_f32 v[56:59], v222, v81, v[56:59]
	v_mfma_f32_4x4x1_16b_f32 v[60:63], v222, v192, v[60:63]
	v_mfma_f32_4x4x1_16b_f32 v[224:227], v222, v193, v[224:227]
	v_cvt_pk_f32_fp8_e32 v[76:77], v122
	v_cvt_pk_f32_fp8_sdwa v[78:79], v122 src0_sel:WORD_1
	s_waitcnt lgkmcnt(0)
	v_cvt_pk_f32_fp8_e32 v[80:81], v123
	v_cvt_pk_f32_fp8_sdwa v[188:189], v123 src0_sel:WORD_1
	v_mfma_f32_4x4x1_16b_f32 v[36:39], v223, v76, v[36:39]
	v_mfma_f32_4x4x1_16b_f32 v[40:43], v223, v77, v[40:43]
	v_mfma_f32_4x4x1_16b_f32 v[44:47], v223, v78, v[44:47]
	v_mfma_f32_4x4x1_16b_f32 v[48:51], v223, v79, v[48:51]
	v_mfma_f32_4x4x1_16b_f32 v[52:55], v223, v80, v[52:55]
	v_mfma_f32_4x4x1_16b_f32 v[56:59], v223, v81, v[56:59]
	v_mfma_f32_4x4x1_16b_f32 v[60:63], v223, v188, v[60:63]
	v_mfma_f32_4x4x1_16b_f32 v[224:227], v223, v189, v[224:227]
	ds_read_b32 v220, v236 offset:1792
	ds_read_b32 v221, v236 offset:1856
	v_cvt_pk_f32_fp8_e32 v[80:81], v137
	v_cvt_pk_f32_fp8_sdwa v[192:193], v137 src0_sel:WORD_1
	s_waitcnt lgkmcnt(1)
	v_cvt_pk_f32_fp8_e32 v[76:77], v136
	v_mfma_f32_4x4x1_16b_f32 v[52:55], v220, v80, v[52:55]
	v_mfma_f32_4x4x1_16b_f32 v[56:59], v220, v81, v[56:59]
	v_cvt_pk_f32_fp8_e32 v[80:81], v135
	v_mfma_f32_4x4x1_16b_f32 v[36:39], v220, v76, v[36:39]
	v_mfma_f32_4x4x1_16b_f32 v[40:43], v220, v77, v[40:43]
	v_mfma_f32_4x4x1_16b_f32 v[60:63], v220, v192, v[60:63]
	s_waitcnt lgkmcnt(0)
	v_cvt_pk_f32_fp8_e32 v[76:77], v134
	v_mfma_f32_4x4x1_16b_f32 v[52:55], v221, v80, v[52:55]
	v_cvt_pk_f32_fp8_sdwa v[78:79], v136 src0_sel:WORD_1
	v_mfma_f32_4x4x1_16b_f32 v[36:39], v221, v76, v[36:39]
	s_nop 0
	v_mfma_f32_4x4x1_16b_f32 v[44:47], v220, v78, v[44:47]
	v_mfma_f32_4x4x1_16b_f32 v[48:51], v220, v79, v[48:51]
	v_cvt_pk_f32_fp8_sdwa v[78:79], v134 src0_sel:WORD_1
	v_mfma_f32_4x4x1_16b_f32 v[56:59], v221, v81, v[56:59]
	v_mfma_f32_4x4x1_16b_f32 v[224:227], v220, v193, v[224:227]
	v_cvt_pk_f32_fp8_sdwa v[188:189], v135 src0_sel:WORD_1
	v_mfma_f32_4x4x1_16b_f32 v[40:43], v221, v77, v[40:43]
	v_mfma_f32_4x4x1_16b_f32 v[44:47], v221, v78, v[44:47]
	v_mfma_f32_4x4x1_16b_f32 v[48:51], v221, v79, v[48:51]
	ds_read_b32 v222, v236 offset:1920
	v_mfma_f32_4x4x1_16b_f32 v[60:63], v221, v188, v[60:63]
	v_mfma_f32_4x4x1_16b_f32 v[224:227], v221, v189, v[224:227]
	ds_read_b32 v223, v236 offset:1984
	v_cvt_pk_f32_fp8_e32 v[80:81], v133
	v_cvt_pk_f32_fp8_sdwa v[192:193], v133 src0_sel:WORD_1
	s_waitcnt lgkmcnt(1)
	v_cvt_pk_f32_fp8_e32 v[76:77], v132
	v_cvt_pk_f32_fp8_sdwa v[78:79], v132 src0_sel:WORD_1
	s_nop 0
	v_mfma_f32_4x4x1_16b_f32 v[36:39], v222, v76, v[36:39]
	v_mfma_f32_4x4x1_16b_f32 v[40:43], v222, v77, v[40:43]
	v_mfma_f32_4x4x1_16b_f32 v[44:47], v222, v78, v[44:47]
	v_mfma_f32_4x4x1_16b_f32 v[48:51], v222, v79, v[48:51]
	v_mfma_f32_4x4x1_16b_f32 v[52:55], v222, v80, v[52:55]
	v_mfma_f32_4x4x1_16b_f32 v[56:59], v222, v81, v[56:59]
	v_mfma_f32_4x4x1_16b_f32 v[60:63], v222, v192, v[60:63]
	v_mfma_f32_4x4x1_16b_f32 v[224:227], v222, v193, v[224:227]
	v_cvt_pk_f32_fp8_e32 v[76:77], v130
	v_cvt_pk_f32_fp8_sdwa v[78:79], v130 src0_sel:WORD_1
	s_waitcnt lgkmcnt(0)
	v_cvt_pk_f32_fp8_e32 v[80:81], v131
	v_cvt_pk_f32_fp8_sdwa v[188:189], v131 src0_sel:WORD_1
	v_mfma_f32_4x4x1_16b_f32 v[36:39], v223, v76, v[36:39]
	v_mfma_f32_4x4x1_16b_f32 v[40:43], v223, v77, v[40:43]
	v_mfma_f32_4x4x1_16b_f32 v[44:47], v223, v78, v[44:47]
	v_mfma_f32_4x4x1_16b_f32 v[48:51], v223, v79, v[48:51]
	v_mfma_f32_4x4x1_16b_f32 v[52:55], v223, v80, v[52:55]
	v_mfma_f32_4x4x1_16b_f32 v[56:59], v223, v81, v[56:59]
	v_mfma_f32_4x4x1_16b_f32 v[60:63], v223, v188, v[60:63]
	v_mfma_f32_4x4x1_16b_f32 v[224:227], v223, v189, v[224:227]

.LBB0_1245:
	s_nop 4
	s_waitcnt vmcnt(15)
	ds_bpermute_b32 v2, v168, v36
	ds_bpermute_b32 v3, v168, v40
	s_waitcnt vmcnt(13)
	ds_bpermute_b32 v6, v168, v44
	ds_bpermute_b32 v7, v168, v48
	s_waitcnt vmcnt(11)
	ds_bpermute_b32 v10, v168, v52
	ds_bpermute_b32 v11, v168, v56
	s_waitcnt vmcnt(9)
	ds_bpermute_b32 v14, v168, v60
	ds_bpermute_b32 v15, v168, v224
	s_waitcnt vmcnt(7)
	ds_bpermute_b32 v18, v168, v37
	ds_bpermute_b32 v19, v168, v41
	s_waitcnt vmcnt(5)
	ds_bpermute_b32 v22, v168, v45
	ds_bpermute_b32 v23, v168, v49
	s_waitcnt vmcnt(3)
	ds_bpermute_b32 v28, v168, v53
	ds_bpermute_b32 v29, v168, v57
	s_waitcnt vmcnt(1)
	ds_bpermute_b32 v32, v168, v61
	ds_bpermute_b32 v33, v168, v225
	s_waitcnt lgkmcnt(14)
	v_add_f32_e32 v2, v36, v2
	v_add_f32_e32 v3, v40, v3
	s_waitcnt lgkmcnt(12)
	v_add_f32_e32 v6, v44, v6
	v_add_f32_e32 v7, v48, v7
	s_waitcnt lgkmcnt(10)
	v_add_f32_e32 v10, v52, v10
	v_add_f32_e32 v11, v56, v11
	s_waitcnt lgkmcnt(8)
	v_add_f32_e32 v14, v60, v14
	v_add_f32_e32 v15, v224, v15
	s_waitcnt lgkmcnt(6)
	v_add_f32_e32 v18, v37, v18
	v_add_f32_e32 v19, v41, v19
	s_waitcnt lgkmcnt(4)
	v_add_f32_e32 v22, v45, v22
	v_add_f32_e32 v23, v49, v23
	s_waitcnt lgkmcnt(2)
	v_add_f32_e32 v28, v53, v28
	v_add_f32_e32 v29, v57, v29
	s_waitcnt lgkmcnt(0)
	v_add_f32_e32 v32, v61, v32
	v_add_f32_e32 v33, v225, v33
	ds_bpermute_b32 v36, v168, v38
	ds_bpermute_b32 v40, v168, v42
	ds_bpermute_b32 v44, v168, v46
	ds_bpermute_b32 v48, v168, v50
	ds_bpermute_b32 v52, v168, v54
	ds_bpermute_b32 v56, v168, v58
	ds_bpermute_b32 v60, v168, v62
	ds_bpermute_b32 v224, v168, v226
	ds_bpermute_b32 v37, v168, v39
	ds_bpermute_b32 v41, v168, v43
	ds_bpermute_b32 v45, v168, v47
	ds_bpermute_b32 v49, v168, v51
	ds_bpermute_b32 v53, v168, v55
	ds_bpermute_b32 v57, v168, v59
	ds_bpermute_b32 v61, v168, v63
	ds_bpermute_b32 v225, v168, v227
	s_waitcnt lgkmcnt(14)
	v_add_f32_e32 v38, v38, v36
	v_add_f32_e32 v42, v42, v40
	s_waitcnt lgkmcnt(12)
	v_add_f32_e32 v46, v46, v44
	v_add_f32_e32 v50, v50, v48
	s_waitcnt lgkmcnt(10)
	v_add_f32_e32 v54, v54, v52
	v_add_f32_e32 v58, v58, v56
	s_waitcnt lgkmcnt(8)
	v_add_f32_e32 v62, v62, v60
	v_add_f32_e32 v226, v226, v224
	s_waitcnt lgkmcnt(6)
	v_add_f32_e32 v39, v39, v37
	v_add_f32_e32 v43, v43, v41
	s_waitcnt lgkmcnt(4)
	v_add_f32_e32 v47, v47, v45
	v_add_f32_e32 v51, v51, v49
	s_waitcnt lgkmcnt(2)
	v_add_f32_e32 v55, v55, v53
	v_add_f32_e32 v59, v59, v57
	s_waitcnt lgkmcnt(0)
	v_add_f32_e32 v63, v63, v61
	v_add_f32_e32 v227, v227, v225
	ds_bpermute_b32 v4, v167, v2
	ds_bpermute_b32 v5, v167, v3
	ds_bpermute_b32 v8, v167, v6
	ds_bpermute_b32 v9, v167, v7
	ds_bpermute_b32 v12, v167, v10
	ds_bpermute_b32 v13, v167, v11
	ds_bpermute_b32 v16, v167, v14
	ds_bpermute_b32 v17, v167, v15
	ds_bpermute_b32 v20, v167, v18
	ds_bpermute_b32 v21, v167, v19
	ds_bpermute_b32 v24, v167, v22
	ds_bpermute_b32 v25, v167, v23
	ds_bpermute_b32 v30, v167, v28
	ds_bpermute_b32 v31, v167, v29
	s_waitcnt vmcnt(0)
	ds_bpermute_b32 v34, v167, v32
	ds_bpermute_b32 v35, v167, v33
	ds_bpermute_b32 v36, v167, v38
	ds_bpermute_b32 v40, v167, v42
	ds_bpermute_b32 v44, v167, v46
	ds_bpermute_b32 v48, v167, v50
	ds_bpermute_b32 v52, v167, v54
	ds_bpermute_b32 v56, v167, v58
	ds_bpermute_b32 v60, v167, v62
	ds_bpermute_b32 v224, v167, v226
	ds_bpermute_b32 v37, v167, v39
	ds_bpermute_b32 v41, v167, v43
	ds_bpermute_b32 v45, v167, v47
	ds_bpermute_b32 v49, v167, v51
	ds_bpermute_b32 v53, v167, v55
	ds_bpermute_b32 v57, v167, v59
	ds_bpermute_b32 v61, v167, v63
	ds_bpermute_b32 v225, v167, v227
	s_and_saveexec_b64 s[2:3], s[6:7]
	s_cbranch_execz .LBB0_1193
	v_add_f32_e32 v67, v66, v67
	v_add_f32_e32 v69, v68, v69
	v_add_f32_e32 v66, v72, v73
	v_rcp_f32_e32 v72, v67
	v_add_f32_e32 v68, v70, v71
	v_rcp_f32_e32 v70, v69
	v_rcp_f32_e32 v68, v68
	v_rcp_f32_e32 v66, v66
	s_lshl_b32 s20, s37, 12
	v_lshl_add_u64 v[64:65], v[120:121], 0, s[20:21]
	s_waitcnt lgkmcnt(0)
	v_add_f32_e32 v2, v2, v4
	v_add_f32_e32 v3, v3, v5
	v_add_f32_e32 v6, v6, v8
	v_add_f32_e32 v7, v7, v9
	v_add_f32_e32 v10, v10, v12
	v_add_f32_e32 v11, v11, v13
	v_add_f32_e32 v14, v14, v16
	v_add_f32_e32 v15, v15, v17
	v_mul_f32_e32 v2, v72, v2
	v_mul_f32_e32 v3, v72, v3
	v_mul_f32_e32 v6, v72, v6
	v_mul_f32_e32 v7, v72, v7
	v_mul_f32_e32 v10, v72, v10
	v_mul_f32_e32 v11, v72, v11
	v_mul_f32_e32 v14, v72, v14
	v_mul_f32_e32 v15, v72, v15
	v_cvt_pk_bf16_f32 v2, v2, v3
	v_cvt_pk_bf16_f32 v3, v6, v7
	v_cvt_pk_bf16_f32 v4, v10, v11
	v_cvt_pk_bf16_f32 v5, v14, v15
	global_store_dwordx4 v[64:65], v[2:5], off
	v_add_f32_e32 v18, v18, v20
	v_add_f32_e32 v19, v19, v21
	v_add_f32_e32 v22, v22, v24
	v_add_f32_e32 v23, v23, v25
	v_add_f32_e32 v28, v28, v30
	v_add_f32_e32 v29, v29, v31
	v_add_f32_e32 v32, v32, v34
	v_add_f32_e32 v33, v33, v35
	v_mul_f32_e32 v18, v70, v18
	v_mul_f32_e32 v19, v70, v19
	v_mul_f32_e32 v22, v70, v22
	v_mul_f32_e32 v23, v70, v23
	v_mul_f32_e32 v28, v70, v28
	v_mul_f32_e32 v29, v70, v29
	v_mul_f32_e32 v32, v70, v32
	v_mul_f32_e32 v33, v70, v33
	v_cvt_pk_bf16_f32 v18, v18, v19
	v_cvt_pk_bf16_f32 v19, v22, v23
	v_cvt_pk_bf16_f32 v20, v28, v29
	v_cvt_pk_bf16_f32 v21, v32, v33
	global_store_dwordx4 v[64:65], v[18:21], off offset:256
	v_add_f32_e32 v38, v38, v36
	v_add_f32_e32 v42, v42, v40
	v_add_f32_e32 v46, v46, v44
	v_add_f32_e32 v50, v50, v48
	v_add_f32_e32 v54, v54, v52
	v_add_f32_e32 v58, v58, v56
	v_add_f32_e32 v62, v62, v60
	v_add_f32_e32 v226, v226, v224
	v_mul_f32_e32 v38, v68, v38
	v_mul_f32_e32 v42, v68, v42
	v_mul_f32_e32 v46, v68, v46
	v_mul_f32_e32 v50, v68, v50
	v_mul_f32_e32 v54, v68, v54
	v_mul_f32_e32 v58, v68, v58
	v_mul_f32_e32 v62, v68, v62
	v_mul_f32_e32 v226, v68, v226
	v_cvt_pk_bf16_f32 v8, v38, v42
	v_cvt_pk_bf16_f32 v9, v46, v50
	v_cvt_pk_bf16_f32 v10, v54, v58
	v_cvt_pk_bf16_f32 v11, v62, v226
	global_store_dwordx4 v[64:65], v[8:11], off offset:512
	v_add_f32_e32 v39, v39, v37
	v_add_f32_e32 v43, v43, v41
	v_add_f32_e32 v47, v47, v45
	v_add_f32_e32 v51, v51, v49
	v_add_f32_e32 v55, v55, v53
	v_add_f32_e32 v59, v59, v57
	v_add_f32_e32 v63, v63, v61
	v_add_f32_e32 v227, v227, v225
	v_mul_f32_e32 v39, v66, v39
	v_mul_f32_e32 v43, v66, v43
	v_mul_f32_e32 v47, v66, v47
	v_mul_f32_e32 v51, v66, v51
	v_mul_f32_e32 v55, v66, v55
	v_mul_f32_e32 v59, v66, v59
	v_mul_f32_e32 v63, v66, v63
	v_mul_f32_e32 v227, v66, v227
	v_cvt_pk_bf16_f32 v12, v39, v43
	v_cvt_pk_bf16_f32 v13, v47, v51
	v_cvt_pk_bf16_f32 v14, v55, v59
	v_cvt_pk_bf16_f32 v15, v63, v227
	global_store_dwordx4 v[64:65], v[12:15], off offset:768
	s_branch .LBB0_1193
